# baseline (speedup 1.0000x reference)
_Z9proj_gemmPKfS0_S0_PK14__hip_bfloat16S0_S0_S0_PS1_:
	s_lshl_b32 s3, s2, 2
	s_load_dwordx8 s[8:15], s[0:1], 0x0
	s_and_b32 s3, s3, 28
	s_bfe_u32 s30, s2, 0x20005
	s_lshr_b32 s6, s2, 3
	s_ashr_i32 s18, s2, 7
	s_lshr_b32 s7, s2, 5
	s_or_b32 s20, s3, s30
	s_bfe_u32 s3, s2, 0x20003
	s_cmpk_lt_u32 s2, 0x80
	s_cselect_b64 s[16:17], -1, 0
	s_and_b64 s[4:5], s[16:17], exec
	s_waitcnt lgkmcnt(0)
	s_cselect_b32 s4, s9, s11
	s_cselect_b32 s5, s8, s10
	s_lshl_b32 s24, s20, 18
	s_lshl_b32 s8, s20, 20
	s_add_u32 s25, s5, s8
	s_addc_u32 s26, s4, 0
	s_ashr_i32 s19, s18, 31
	s_lshl_b64 s[4:5], s[18:19], 21
	s_add_u32 s4, s14, s4
	s_addc_u32 s5, s15, s5
	s_lshl_b32 s8, s3, 19
	s_add_u32 s27, s4, s8
	s_addc_u32 s28, s5, 0
	s_xor_b32 s6, s6, s18
	v_lshlrev_b32_e32 v1, 4, v0
	s_lshl_b32 s34, s6, 4
	v_lshlrev_b32_e32 v2, 3, v0
	v_and_b32_e32 v3, 0x1f0, v1
	s_movk_i32 s6, 0x200
	s_lshl_b32 s4, s20, 1
	s_mul_i32 s31, s18, 5
	s_xor_b32 s7, s7, s18
	v_lshrrev_b32_e32 v28, 6, v0
	s_and_b32 s35, s34, 16
	v_and_or_b32 v29, v2, s6, v3
	v_lshrrev_b32_e32 v2, 1, v0
	v_and_b32_e32 v3, 48, v1
	s_add_i32 s4, s4, s31
	v_bitop3_b32 v2, v2, v3, 32 bitop3:0x6c
	v_or_b32_e32 v30, s35, v28
	s_lshl_b32 s38, s7, 4
	s_and_b32 s5, s4, 15
	v_lshrrev_b32_e32 v2, 1, v2
	v_or_b32_e32 v32, 8, v30
	s_and_b32 s39, s38, 16
	v_and_or_b32 v178, v0, 32, v2
	v_lshlrev_b32_e32 v2, 3, v30
	v_lshrrev_b32_e32 v31, 6, v29
	s_movk_i32 s36, 0xb0
	v_lshlrev_b32_e32 v3, 3, v32
	s_movk_i32 s37, 0xf0
	v_or_b32_e32 v33, s39, v28
	s_lshl_b32 s33, s4, 6
	s_lshl_b32 s4, s5, 8
	v_and_or_b32 v2, v2, s36, v31
	v_and_or_b32 v12, v3, s37, v31
	v_lshlrev_b32_e32 v3, 3, v33
	v_or_b32_e32 v34, 8, v33
	s_add_u32 s20, s25, s4
	v_mov_b32_e32 v183, 0
	v_and_or_b32 v20, v3, s36, v31
	v_lshlrev_b32_e32 v3, 3, v34
	s_addc_u32 s21, s26, 0
	v_lshlrev_b32_e32 v180, 12, v2
	v_mov_b32_e32 v181, v183
	v_and_or_b32 v22, v3, s37, v31
	v_lshl_add_u64 v[2:3], s[20:21], 0, v[180:181]
	v_lshlrev_b32_e32 v182, 2, v178
	v_lshl_add_u64 v[10:11], v[2:3], 0, v[182:183]
	v_lshlrev_b32_e32 v184, 12, v12
	v_mov_b32_e32 v185, v183
	s_lshl_b32 s4, s5, 7
	global_load_dwordx4 v[2:5], v[10:11], off offset:16
	global_load_dwordx4 v[6:9], v[10:11], off
	v_lshl_add_u64 v[10:11], s[20:21], 0, v[184:185]
	s_add_u32 s22, s27, s4
	v_lshl_add_u64 v[14:15], v[10:11], 0, v[182:183]
	s_addc_u32 s23, s28, 0
	v_lshlrev_b32_e32 v186, 11, v20
	v_mov_b32_e32 v187, v183
	global_load_dwordx4 v[10:13], v[14:15], off offset:16
	global_load_dwordx4 v[16:19], v[14:15], off
	v_lshl_add_u64 v[20:21], s[22:23], 0, v[186:187]
	v_lshlrev_b32_e32 v14, 1, v178
	v_mov_b32_e32 v15, v183
	v_lshlrev_b32_e32 v188, 11, v22
	v_mov_b32_e32 v189, v183
	v_lshl_add_u64 v[24:25], v[20:21], 0, v[14:15]
	v_lshl_add_u64 v[20:21], s[22:23], 0, v[188:189]
	v_lshl_add_u64 v[26:27], v[20:21], 0, v[14:15]
	global_load_dwordx4 v[20:23], v[24:25], off
	global_load_dwordx4 v[50:53], v[26:27], off
	v_bfe_u32 v24, v0, 5, 1
	v_and_or_b32 v25, v30, 22, v24
	v_lshl_or_b32 v208, v25, 10, v29
	v_and_or_b32 v25, v32, 30, v24
	v_lshl_or_b32 v205, v25, 10, v29
	v_bitop3_b32 v25, s34, 16, v28 bitop3:0x26
	v_and_or_b32 v26, v25, 22, v24
	v_lshl_or_b32 v204, v26, 10, v29
	v_bitop3_b32 v26, s35, v28, 24 bitop3:0xde
	v_and_or_b32 v27, v26, 30, v24
	v_lshl_or_b32 v201, v27, 10, v29
	v_and_or_b32 v27, v33, 22, v24
	v_lshl_or_b32 v206, v27, 10, v29
	v_and_or_b32 v27, v34, 30, v24
	s_load_dwordx8 s[4:11], s[0:1], 0x20
	v_lshl_or_b32 v207, v27, 10, v29
	v_bitop3_b32 v27, s38, 16, v28 bitop3:0x26
	v_bitop3_b32 v28, s39, v28, 24 bitop3:0xde
	v_and_or_b32 v30, v27, 22, v24
	v_and_or_b32 v24, v28, 30, v24
	v_and_b32_e32 v179, 15, v0
	v_lshl_or_b32 v202, v30, 10, v29
	v_lshl_or_b32 v203, v24, 10, v29
	v_lshlrev_b32_e32 v24, 3, v28
	v_lshlrev_b32_e32 v29, 2, v0
	v_lshrrev_b32_e32 v198, 8, v0
	v_lshlrev_b32_e32 v25, 3, v25
	v_lshlrev_b32_e32 v26, 3, v26
	v_lshlrev_b32_e32 v27, 3, v27
	v_and_or_b32 v28, v24, s37, v31
	v_and_b32_e32 v24, 48, v0
	v_and_b32_e32 v29, 32, v29
	v_lshlrev_b32_e32 v30, 6, v179
	s_mov_b32 s29, 0
	v_and_b32_e32 v199, 63, v0
	v_and_or_b32 v25, v25, s36, v31
	v_and_or_b32 v26, v26, s37, v31
	v_bfe_u32 v200, v0, 6, 2
	v_and_or_b32 v27, v27, s36, v31
	v_lshlrev_b32_e32 v80, 14, v198
	v_bitop3_b32 v81, v30, v29, v24 bitop3:0x36
	v_lshlrev_b32_e32 v190, 12, v25
	v_mov_b32_e32 v191, v183
	v_lshl_add_u64 v[24:25], s[20:21], 0, v[190:191]
	v_lshl_add_u64 v[24:25], v[24:25], 0, v[182:183]
	v_lshlrev_b32_e32 v192, 12, v26
	v_mov_b32_e32 v193, v183
	global_load_dwordx4 v[54:57], v[24:25], off offset:16
	global_load_dwordx4 v[58:61], v[24:25], off
	v_lshl_add_u64 v[24:25], s[20:21], 0, v[192:193]
	v_lshl_add_u64 v[24:25], v[24:25], 0, v[182:183]
	v_lshlrev_b32_e32 v194, 11, v27
	v_mov_b32_e32 v195, v183
	global_load_dwordx4 v[62:65], v[24:25], off offset:16
	global_load_dwordx4 v[66:69], v[24:25], off
	v_lshl_add_u64 v[24:25], s[22:23], 0, v[194:195]
	v_lshlrev_b32_e32 v196, 11, v28
	v_mov_b32_e32 v197, v183
	v_lshl_add_u64 v[24:25], v[24:25], 0, v[14:15]
	v_lshl_add_u64 v[26:27], s[22:23], 0, v[196:197]
	v_lshl_add_u64 v[26:27], v[26:27], 0, v[14:15]
	global_load_dwordx4 v[70:73], v[24:25], off
	global_load_dwordx4 v[74:77], v[26:27], off
	s_add_i32 s33, s33, 64
	s_and_b32 s20, s33, 0x3c0
	s_lshl_b32 s0, s20, 2
	s_add_u32 s0, s25, s0
	s_addc_u32 s1, s26, 0
	v_lshl_add_u64 v[24:25], s[0:1], 0, v[180:181]
	v_lshl_add_u64 v[24:25], v[24:25], 0, v[182:183]
	s_lshl_b32 s20, s20, 1
	global_load_dwordx4 v[42:45], v[24:25], off offset:16
	global_load_dwordx4 v[46:49], v[24:25], off
	v_lshl_add_u64 v[24:25], s[0:1], 0, v[184:185]
	s_add_u32 s20, s27, s20
	v_lshl_add_u64 v[24:25], v[24:25], 0, v[182:183]
	s_addc_u32 s21, s28, 0
	global_load_dwordx4 v[34:37], v[24:25], off offset:16
	global_load_dwordx4 v[38:41], v[24:25], off
	v_lshl_add_u64 v[24:25], s[20:21], 0, v[186:187]
	v_lshl_add_u64 v[24:25], v[24:25], 0, v[14:15]
	v_lshl_add_u64 v[26:27], s[20:21], 0, v[188:189]
	v_lshl_add_u64 v[78:79], v[26:27], 0, v[14:15]
	global_load_dwordx4 v[30:33], v[24:25], off
	global_load_dwordx4 v[26:29], v[78:79], off
	s_waitcnt vmcnt(16)
	v_cvt_pk_bf16_f32 v6, v6, v7
	v_cvt_pk_bf16_f32 v7, v8, v9
	v_cvt_pk_bf16_f32 v8, v2, v3
	v_add_u32_e32 v2, 0, v208
	v_cvt_pk_bf16_f32 v9, v4, v5
	ds_write_b128 v2, v[6:9]
	s_waitcnt vmcnt(14)
	v_cvt_pk_bf16_f32 v2, v16, v17
	v_add_u32_e32 v6, 0, v205
	v_cvt_pk_bf16_f32 v3, v18, v19
	v_cvt_pk_bf16_f32 v4, v10, v11
	v_cvt_pk_bf16_f32 v5, v12, v13
	ds_write_b128 v6, v[2:5]
	v_add_u32_e32 v2, 0, v206
	s_waitcnt vmcnt(13)
	ds_write_b128 v2, v[20:23] offset:32768
	v_add_u32_e32 v2, 0, v207
	s_waitcnt vmcnt(12)
	ds_write_b128 v2, v[50:53] offset:32768
	s_waitcnt vmcnt(10)
	v_cvt_pk_bf16_f32 v2, v58, v59
	v_add_u32_e32 v6, 0, v204
	v_cvt_pk_bf16_f32 v3, v60, v61
	v_cvt_pk_bf16_f32 v4, v54, v55
	v_cvt_pk_bf16_f32 v5, v56, v57
	ds_write_b128 v6, v[2:5]
	s_waitcnt vmcnt(8)
	v_cvt_pk_bf16_f32 v2, v66, v67
	v_add_u32_e32 v6, 0, v201
	v_cvt_pk_bf16_f32 v3, v68, v69
	v_cvt_pk_bf16_f32 v4, v62, v63
	v_cvt_pk_bf16_f32 v5, v64, v65
	ds_write_b128 v6, v[2:5]
	v_add_u32_e32 v2, 0, v202
	s_waitcnt vmcnt(7)
	ds_write_b128 v2, v[70:73] offset:32768
	v_add_u32_e32 v2, 0, v203
	s_waitcnt vmcnt(6)
	ds_write_b128 v2, v[74:77] offset:32768
	v_lshl_add_u64 v[2:3], s[0:1], 0, v[190:191]
	v_lshl_add_u64 v[2:3], v[2:3], 0, v[182:183]
	global_load_dwordx4 v[6:9], v[2:3], off offset:16
	global_load_dwordx4 v[22:25], v[2:3], off
	v_lshl_add_u64 v[2:3], s[0:1], 0, v[192:193]
	v_lshl_add_u64 v[16:17], v[2:3], 0, v[182:183]
	global_load_dwordx4 v[2:5], v[16:17], off offset:16
	global_load_dwordx4 v[10:13], v[16:17], off
	v_lshl_add_u64 v[16:17], s[20:21], 0, v[194:195]
	v_lshl_add_u64 v[50:51], v[16:17], 0, v[14:15]
	v_lshl_add_u64 v[16:17], s[20:21], 0, v[196:197]
	v_lshl_add_u64 v[52:53], v[16:17], 0, v[14:15]
	global_load_dwordx4 v[18:21], v[50:51], off
	global_load_dwordx4 v[14:17], v[52:53], off
	v_lshlrev_b32_e32 v50, 13, v200
	s_cmp_lg_u32 0, -1
	s_cselect_b32 s0, 0, 0
	v_add3_u32 v209, v80, s0, v81
	s_add_i32 s0, s0, 0x8000
	v_add3_u32 v210, v50, s0, v81
	s_lshl_b32 s0, s30, 1
	s_add_i32 s31, s31, s0
	s_lshl_b32 s0, s2, 3
	s_add_i32 s0, s0, s31
	s_waitcnt lgkmcnt(0)
	s_and_b32 s0, s0, 15
	s_lshl_b32 s0, s0, 6
	s_add_i32 s22, s0, 0x80
	v_mov_b32_e32 v50, v183
	v_mov_b32_e32 v51, v183
	v_mov_b32_e32 v52, v183
	v_mov_b32_e32 v53, v183
	v_mov_b32_e32 v54, v183
	v_mov_b32_e32 v55, v183
	v_mov_b32_e32 v56, v183
	v_mov_b32_e32 v57, v183
	v_mov_b32_e32 v58, v183
	v_mov_b32_e32 v59, v183
	v_mov_b32_e32 v60, v183
	v_mov_b32_e32 v61, v183
	v_mov_b32_e32 v62, v183
	v_mov_b32_e32 v63, v183
	v_mov_b32_e32 v64, v183
	v_mov_b32_e32 v65, v183
	v_mov_b32_e32 v66, v183
	v_mov_b32_e32 v67, v183
	v_mov_b32_e32 v68, v183
	v_mov_b32_e32 v69, v183
	v_mov_b32_e32 v70, v183
	v_mov_b32_e32 v71, v183
	v_mov_b32_e32 v72, v183
	v_mov_b32_e32 v73, v183
	v_mov_b32_e32 v74, v183
	v_mov_b32_e32 v75, v183
	v_mov_b32_e32 v76, v183
	v_mov_b32_e32 v77, v183
	v_mov_b32_e32 v78, v183
	v_mov_b32_e32 v79, v183
	v_mov_b32_e32 v80, v183
	v_mov_b32_e32 v81, v183
	v_mov_b32_e32 v82, v183
	v_mov_b32_e32 v83, v183
	v_mov_b32_e32 v84, v183
	v_mov_b32_e32 v85, v183
	v_mov_b32_e32 v86, v183
	v_mov_b32_e32 v87, v183
	v_mov_b32_e32 v88, v183
	v_mov_b32_e32 v89, v183
	v_mov_b32_e32 v90, v183
	v_mov_b32_e32 v91, v183
	v_mov_b32_e32 v92, v183
	v_mov_b32_e32 v93, v183
	v_mov_b32_e32 v94, v183
	v_mov_b32_e32 v95, v183
	v_mov_b32_e32 v96, v183
	v_mov_b32_e32 v97, v183
	v_mov_b32_e32 v98, v183
	v_mov_b32_e32 v99, v183
	v_mov_b32_e32 v100, v183
	v_mov_b32_e32 v101, v183
	v_mov_b32_e32 v102, v183
	v_mov_b32_e32 v103, v183
	v_mov_b32_e32 v104, v183
	v_mov_b32_e32 v105, v183
	v_mov_b32_e32 v106, v183
	v_mov_b32_e32 v107, v183
	v_mov_b32_e32 v108, v183
	v_mov_b32_e32 v109, v183
	v_mov_b32_e32 v110, v183
	v_mov_b32_e32 v111, v183
	v_mov_b32_e32 v112, v183
	v_mov_b32_e32 v113, v183
	v_mov_b32_e32 v114, v183
	v_mov_b32_e32 v115, v183
	v_mov_b32_e32 v116, v183
	v_mov_b32_e32 v117, v183
	v_mov_b32_e32 v118, v183
	v_mov_b32_e32 v119, v183
	v_mov_b32_e32 v120, v183
	v_mov_b32_e32 v121, v183
	v_mov_b32_e32 v122, v183
	v_mov_b32_e32 v123, v183
	v_mov_b32_e32 v124, v183
	v_mov_b32_e32 v125, v183
	v_mov_b32_e32 v126, v183
	v_mov_b32_e32 v127, v183
	v_mov_b32_e32 v128, v183
	v_mov_b32_e32 v129, v183
	v_mov_b32_e32 v130, v183
	v_mov_b32_e32 v131, v183
	v_mov_b32_e32 v132, v183
	v_mov_b32_e32 v133, v183
	v_mov_b32_e32 v134, v183
	v_mov_b32_e32 v135, v183
	v_mov_b32_e32 v136, v183
	v_mov_b32_e32 v137, v183
	v_mov_b32_e32 v138, v183
	v_mov_b32_e32 v139, v183
	v_mov_b32_e32 v140, v183
	v_mov_b32_e32 v141, v183
	v_mov_b32_e32 v142, v183
	v_mov_b32_e32 v143, v183
	v_mov_b32_e32 v144, v183
	v_mov_b32_e32 v145, v183
	v_mov_b32_e32 v146, v183
	v_mov_b32_e32 v147, v183
	v_mov_b32_e32 v148, v183
	v_mov_b32_e32 v149, v183
	v_mov_b32_e32 v150, v183
	v_mov_b32_e32 v151, v183
	v_mov_b32_e32 v152, v183
	v_mov_b32_e32 v153, v183
	v_mov_b32_e32 v154, v183
	v_mov_b32_e32 v155, v183
	v_mov_b32_e32 v156, v183
	v_mov_b32_e32 v157, v183
	v_mov_b32_e32 v158, v183
	v_mov_b32_e32 v159, v183
	v_mov_b32_e32 v160, v183
	v_mov_b32_e32 v161, v183
	v_mov_b32_e32 v162, v183
	v_mov_b32_e32 v163, v183
	v_mov_b32_e32 v164, v183
	v_mov_b32_e32 v165, v183
	v_mov_b32_e32 v166, v183
	v_mov_b32_e32 v167, v183
	v_mov_b32_e32 v168, v183
	v_mov_b32_e32 v169, v183
	v_mov_b32_e32 v170, v183
	v_mov_b32_e32 v171, v183
	v_mov_b32_e32 v172, v183
	v_mov_b32_e32 v173, v183
	v_mov_b32_e32 v174, v183
	v_mov_b32_e32 v175, v183
	v_mov_b32_e32 v176, v183
	v_mov_b32_e32 v177, v183
	v_lshlrev_b32_e32 v252, 2, v178
	v_lshlrev_b32_e32 v253, 1, v178
	v_add_u32_e32 v244, v180, v252
	v_add_u32_e32 v245, v184, v252
	v_add_u32_e32 v246, v186, v253
	v_add_u32_e32 v247, v188, v253
	v_add_u32_e32 v248, v190, v252
	v_add_u32_e32 v249, v192, v252
	v_add_u32_e32 v250, v194, v253
	v_add_u32_e32 v251, v196, v253
	s_barrier
.LBB1_1:
	s_and_b32 s0, s29, 0x10000
	v_add_u32_e32 v211, s0, v209
	v_add_u32_e32 v242, s0, v210
	ds_read_b128 v[212:215], v242 offset:0
	ds_read_b128 v[216:219], v242 offset:0x800
	ds_read_b128 v[220:223], v242 offset:0x1000
	ds_read_b128 v[224:227], v242 offset:0x1800
	ds_read_b128 v[228:231], v211 offset:0
	ds_read_b128 v[232:235], v211 offset:0x800
	ds_read_b128 v[236:239], v211 offset:0x1000
	s_waitcnt lgkmcnt(2)
	v_mfma_f32_16x16x32_bf16 v[174:177], v[212:215], v[228:231], v[174:177]
	v_mfma_f32_16x16x32_bf16 v[170:173], v[216:219], v[228:231], v[170:173]
	v_mfma_f32_16x16x32_bf16 v[166:169], v[220:223], v[228:231], v[166:169]
	v_mfma_f32_16x16x32_bf16 v[162:165], v[224:227], v[228:231], v[162:165]
	ds_read_b128 v[228:231], v211 offset:0x1800
	s_waitcnt lgkmcnt(2)
	v_mfma_f32_16x16x32_bf16 v[158:161], v[212:215], v[232:235], v[158:161]
	v_mfma_f32_16x16x32_bf16 v[154:157], v[216:219], v[232:235], v[154:157]
	v_mfma_f32_16x16x32_bf16 v[150:153], v[220:223], v[232:235], v[150:153]
	v_mfma_f32_16x16x32_bf16 v[146:149], v[224:227], v[232:235], v[146:149]
	ds_read_b128 v[232:235], v211 offset:0x2000
	s_waitcnt lgkmcnt(2)
	v_mfma_f32_16x16x32_bf16 v[142:145], v[212:215], v[236:239], v[142:145]
	v_mfma_f32_16x16x32_bf16 v[138:141], v[216:219], v[236:239], v[138:141]
	v_mfma_f32_16x16x32_bf16 v[134:137], v[220:223], v[236:239], v[134:137]
	v_mfma_f32_16x16x32_bf16 v[130:133], v[224:227], v[236:239], v[130:133]
	ds_read_b128 v[236:239], v211 offset:0x2800
	s_waitcnt lgkmcnt(2)
	v_mfma_f32_16x16x32_bf16 v[126:129], v[212:215], v[228:231], v[126:129]
	v_mfma_f32_16x16x32_bf16 v[122:125], v[216:219], v[228:231], v[122:125]
	v_mfma_f32_16x16x32_bf16 v[118:121], v[220:223], v[228:231], v[118:121]
	v_mfma_f32_16x16x32_bf16 v[114:117], v[224:227], v[228:231], v[114:117]
	ds_read_b128 v[228:231], v211 offset:0x3000
	s_waitcnt lgkmcnt(2)
	v_mfma_f32_16x16x32_bf16 v[110:113], v[212:215], v[232:235], v[110:113]
	v_mfma_f32_16x16x32_bf16 v[106:109], v[216:219], v[232:235], v[106:109]
	v_mfma_f32_16x16x32_bf16 v[102:105], v[220:223], v[232:235], v[102:105]
	v_mfma_f32_16x16x32_bf16 v[98:101], v[224:227], v[232:235], v[98:101]
	ds_read_b128 v[232:235], v211 offset:0x3800
	s_waitcnt lgkmcnt(2)
	v_mfma_f32_16x16x32_bf16 v[94:97], v[212:215], v[236:239], v[94:97]
	v_mfma_f32_16x16x32_bf16 v[90:93], v[216:219], v[236:239], v[90:93]
	v_mfma_f32_16x16x32_bf16 v[86:89], v[220:223], v[236:239], v[86:89]
	v_mfma_f32_16x16x32_bf16 v[82:85], v[224:227], v[236:239], v[82:85]
	s_waitcnt lgkmcnt(1)
	v_mfma_f32_16x16x32_bf16 v[78:81], v[212:215], v[228:231], v[78:81]
	v_mfma_f32_16x16x32_bf16 v[74:77], v[216:219], v[228:231], v[74:77]
	v_mfma_f32_16x16x32_bf16 v[70:73], v[220:223], v[228:231], v[70:73]
	v_mfma_f32_16x16x32_bf16 v[66:69], v[224:227], v[228:231], v[66:69]
	s_waitcnt lgkmcnt(0)
	v_mfma_f32_16x16x32_bf16 v[62:65], v[212:215], v[232:235], v[62:65]
	v_mfma_f32_16x16x32_bf16 v[58:61], v[216:219], v[232:235], v[58:61]
	v_mfma_f32_16x16x32_bf16 v[54:57], v[220:223], v[232:235], v[54:57]
	v_mfma_f32_16x16x32_bf16 v[50:53], v[224:227], v[232:235], v[50:53]
	s_xor_b32 s0, s0, 0x10000
	s_and_b32 s1, s22, 0x3c0
	s_add_i32 s23, s0, 0
	s_lshl_b32 s0, s1, 2
	s_add_u32 s20, s25, s0
	s_waitcnt vmcnt(10)
	v_cvt_pk_bf16_f32 v46, v46, v47
	v_cvt_pk_bf16_f32 v47, v48, v49
	v_cvt_pk_bf16_f32 v48, v42, v43
	v_cvt_pk_bf16_f32 v49, v44, v45
	s_waitcnt vmcnt(8)
	v_cvt_pk_bf16_f32 v38, v38, v39
	v_cvt_pk_bf16_f32 v39, v40, v41
	v_cvt_pk_bf16_f32 v40, v34, v35
	v_add_u32_e32 v34, s23, v208
	s_addc_u32 s21, s26, 0
	s_lshl_b32 s0, s1, 1
	v_cvt_pk_bf16_f32 v41, v36, v37
	v_add_u32_e32 v35, s23, v205
	v_add_u32_e32 v36, s23, v206
	v_add_u32_e32 v37, s23, v207
	ds_write_b128 v34, v[46:49]
	ds_write_b128 v35, v[38:41]
	s_waitcnt vmcnt(7)
	ds_write_b128 v36, v[30:33] offset:32768
	s_waitcnt vmcnt(6)
	ds_write_b128 v37, v[26:29] offset:32768
	s_add_u32 s0, s27, s0
	s_addc_u32 s1, s28, 0
	global_load_dwordx4 v[42:45], v244, s[20:21] offset:16
	global_load_dwordx4 v[46:49], v244, s[20:21]
	global_load_dwordx4 v[34:37], v245, s[20:21] offset:16
	global_load_dwordx4 v[38:41], v245, s[20:21]
	global_load_dwordx4 v[30:33], v246, s[0:1]
	global_load_dwordx4 v[26:29], v247, s[0:1]
	ds_read_b128 v[212:215], v242 offset:0x400
	ds_read_b128 v[216:219], v242 offset:0xc00
	ds_read_b128 v[220:223], v242 offset:0x1400
	ds_read_b128 v[224:227], v242 offset:0x1c00
	ds_read_b128 v[228:231], v211 offset:0x400
	ds_read_b128 v[232:235], v211 offset:0xc00
	ds_read_b128 v[236:239], v211 offset:0x1400
	s_waitcnt lgkmcnt(2)
	v_mfma_f32_16x16x32_bf16 v[174:177], v[212:215], v[228:231], v[174:177]
	v_mfma_f32_16x16x32_bf16 v[170:173], v[216:219], v[228:231], v[170:173]
	v_mfma_f32_16x16x32_bf16 v[166:169], v[220:223], v[228:231], v[166:169]
	v_mfma_f32_16x16x32_bf16 v[162:165], v[224:227], v[228:231], v[162:165]
	ds_read_b128 v[228:231], v211 offset:0x1c00
	s_waitcnt lgkmcnt(2)
	v_mfma_f32_16x16x32_bf16 v[158:161], v[212:215], v[232:235], v[158:161]
	v_mfma_f32_16x16x32_bf16 v[154:157], v[216:219], v[232:235], v[154:157]
	v_mfma_f32_16x16x32_bf16 v[150:153], v[220:223], v[232:235], v[150:153]
	v_mfma_f32_16x16x32_bf16 v[146:149], v[224:227], v[232:235], v[146:149]
	ds_read_b128 v[232:235], v211 offset:0x2400
	s_waitcnt lgkmcnt(2)
	v_mfma_f32_16x16x32_bf16 v[142:145], v[212:215], v[236:239], v[142:145]
	v_mfma_f32_16x16x32_bf16 v[138:141], v[216:219], v[236:239], v[138:141]
	v_mfma_f32_16x16x32_bf16 v[134:137], v[220:223], v[236:239], v[134:137]
	v_mfma_f32_16x16x32_bf16 v[130:133], v[224:227], v[236:239], v[130:133]
	ds_read_b128 v[236:239], v211 offset:0x2c00
	s_waitcnt lgkmcnt(2)
	v_mfma_f32_16x16x32_bf16 v[126:129], v[212:215], v[228:231], v[126:129]
	v_mfma_f32_16x16x32_bf16 v[122:125], v[216:219], v[228:231], v[122:125]
	v_mfma_f32_16x16x32_bf16 v[118:121], v[220:223], v[228:231], v[118:121]
	v_mfma_f32_16x16x32_bf16 v[114:117], v[224:227], v[228:231], v[114:117]
	ds_read_b128 v[228:231], v211 offset:0x3400
	s_waitcnt lgkmcnt(2)
	v_mfma_f32_16x16x32_bf16 v[110:113], v[212:215], v[232:235], v[110:113]
	v_mfma_f32_16x16x32_bf16 v[106:109], v[216:219], v[232:235], v[106:109]
	v_mfma_f32_16x16x32_bf16 v[102:105], v[220:223], v[232:235], v[102:105]
	v_mfma_f32_16x16x32_bf16 v[98:101], v[224:227], v[232:235], v[98:101]
	ds_read_b128 v[232:235], v211 offset:0x3c00
	s_waitcnt lgkmcnt(2)
	v_mfma_f32_16x16x32_bf16 v[94:97], v[212:215], v[236:239], v[94:97]
	v_mfma_f32_16x16x32_bf16 v[90:93], v[216:219], v[236:239], v[90:93]
	v_mfma_f32_16x16x32_bf16 v[86:89], v[220:223], v[236:239], v[86:89]
	v_mfma_f32_16x16x32_bf16 v[82:85], v[224:227], v[236:239], v[82:85]
	s_waitcnt lgkmcnt(1)
	v_mfma_f32_16x16x32_bf16 v[78:81], v[212:215], v[228:231], v[78:81]
	v_mfma_f32_16x16x32_bf16 v[74:77], v[216:219], v[228:231], v[74:77]
	v_mfma_f32_16x16x32_bf16 v[70:73], v[220:223], v[228:231], v[70:73]
	v_mfma_f32_16x16x32_bf16 v[66:69], v[224:227], v[228:231], v[66:69]
	s_waitcnt lgkmcnt(0)
	v_mfma_f32_16x16x32_bf16 v[62:65], v[212:215], v[232:235], v[62:65]
	v_mfma_f32_16x16x32_bf16 v[58:61], v[216:219], v[232:235], v[58:61]
	v_mfma_f32_16x16x32_bf16 v[54:57], v[220:223], v[232:235], v[54:57]
	v_mfma_f32_16x16x32_bf16 v[50:53], v[224:227], v[232:235], v[50:53]
	s_waitcnt vmcnt(10)
	v_cvt_pk_bf16_f32 v22, v22, v23
	v_cvt_pk_bf16_f32 v23, v24, v25
	v_cvt_pk_bf16_f32 v24, v6, v7
	v_cvt_pk_bf16_f32 v25, v8, v9
	v_add_u32_e32 v6, s23, v204
	s_waitcnt vmcnt(9)
	v_cvt_pk_bf16_f32 v8, v2, v3
	v_add_u32_e32 v2, s23, v201
	ds_write_b128 v6, v[22:25]
	s_waitcnt vmcnt(8)
	v_cvt_pk_bf16_f32 v6, v10, v11
	v_cvt_pk_bf16_f32 v7, v12, v13
	v_cvt_pk_bf16_f32 v9, v4, v5
	ds_write_b128 v2, v[6:9]
	v_add_u32_e32 v2, s23, v202
	s_waitcnt vmcnt(7)
	ds_write_b128 v2, v[18:21] offset:32768
	v_add_u32_e32 v2, s23, v203
	s_waitcnt vmcnt(6)
	ds_write_b128 v2, v[14:17] offset:32768
	global_load_dwordx4 v[6:9], v248, s[20:21] offset:16
	global_load_dwordx4 v[22:25], v248, s[20:21]
	global_load_dwordx4 v[2:5], v249, s[20:21] offset:16
	global_load_dwordx4 v[10:13], v249, s[20:21]
	global_load_dwordx4 v[18:21], v250, s[0:1]
	global_load_dwordx4 v[14:17], v251, s[0:1]
	s_waitcnt lgkmcnt(0)
	s_add_i32 s22, s22, 64
	s_add_i32 s29, s29, 0x10000
	s_cmp_lg_u32 s29, 0xe0000
	s_barrier
	s_cbranch_scc1 .LBB1_1
	s_lshl_b64 s[0:1], s[18:19], 24
	ds_read_b128 v[180:183], v210 offset:0
	ds_read_b128 v[184:187], v210 offset:0x800
	ds_read_b128 v[188:191], v210 offset:0x1000
	ds_read_b128 v[192:195], v210 offset:0x1800
	ds_read_b128 v[212:215], v209 offset:0
	ds_read_b128 v[216:219], v209 offset:0x800
	ds_read_b128 v[220:223], v209 offset:0x1000
	s_waitcnt lgkmcnt(0)
	s_add_u32 s0, s10, s0
	s_addc_u32 s18, s11, s1
	s_lshl_b32 s19, s24, 1
	s_mov_b32 s1, 0
	s_add_u32 s0, s0, s19
	s_waitcnt lgkmcnt(2)
	s_addc_u32 s20, s18, 0
	v_mfma_f32_16x16x32_bf16 v[174:177], v[180:183], v[212:215], v[174:177]
	v_mfma_f32_16x16x32_bf16 v[170:173], v[184:187], v[212:215], v[170:173]
	v_mfma_f32_16x16x32_bf16 v[166:169], v[188:191], v[212:215], v[166:169]
	v_mfma_f32_16x16x32_bf16 v[162:165], v[192:195], v[212:215], v[162:165]
	ds_read_b128 v[212:215], v209 offset:0x1800
	s_waitcnt lgkmcnt(2)
	s_nop 0
	v_mfma_f32_16x16x32_bf16 v[158:161], v[180:183], v[216:219], v[158:161]
	v_mfma_f32_16x16x32_bf16 v[154:157], v[184:187], v[216:219], v[154:157]
	v_mfma_f32_16x16x32_bf16 v[150:153], v[188:191], v[216:219], v[150:153]
	v_mfma_f32_16x16x32_bf16 v[146:149], v[192:195], v[216:219], v[146:149]
	ds_read_b128 v[216:219], v209 offset:0x2000
	s_waitcnt lgkmcnt(2)
	s_nop 0
	v_mfma_f32_16x16x32_bf16 v[142:145], v[180:183], v[220:223], v[142:145]
	v_mfma_f32_16x16x32_bf16 v[138:141], v[184:187], v[220:223], v[138:141]
	v_mfma_f32_16x16x32_bf16 v[134:137], v[188:191], v[220:223], v[134:137]
	v_mfma_f32_16x16x32_bf16 v[130:133], v[192:195], v[220:223], v[130:133]
	ds_read_b128 v[220:223], v209 offset:0x2800
	s_waitcnt lgkmcnt(2)
	s_nop 0
	v_mfma_f32_16x16x32_bf16 v[126:129], v[180:183], v[212:215], v[126:129]
	v_mfma_f32_16x16x32_bf16 v[122:125], v[184:187], v[212:215], v[122:125]
	v_mfma_f32_16x16x32_bf16 v[118:121], v[188:191], v[212:215], v[118:121]
	v_mfma_f32_16x16x32_bf16 v[114:117], v[192:195], v[212:215], v[114:117]
	ds_read_b128 v[212:215], v209 offset:0x3000
	s_waitcnt lgkmcnt(2)
	s_nop 0
	v_mfma_f32_16x16x32_bf16 v[110:113], v[180:183], v[216:219], v[110:113]
	v_mfma_f32_16x16x32_bf16 v[106:109], v[184:187], v[216:219], v[106:109]
	v_mfma_f32_16x16x32_bf16 v[102:105], v[188:191], v[216:219], v[102:105]
	v_mfma_f32_16x16x32_bf16 v[98:101], v[192:195], v[216:219], v[98:101]
	ds_read_b128 v[216:219], v209 offset:0x3800
	s_waitcnt lgkmcnt(2)
	s_nop 0
	v_mfma_f32_16x16x32_bf16 v[94:97], v[180:183], v[220:223], v[94:97]
	v_mfma_f32_16x16x32_bf16 v[90:93], v[184:187], v[220:223], v[90:93]
	v_mfma_f32_16x16x32_bf16 v[86:89], v[188:191], v[220:223], v[86:89]
	v_mfma_f32_16x16x32_bf16 v[82:85], v[192:195], v[220:223], v[82:85]
	s_waitcnt lgkmcnt(1)
	s_nop 0
	v_mfma_f32_16x16x32_bf16 v[78:81], v[180:183], v[212:215], v[78:81]
	v_mfma_f32_16x16x32_bf16 v[74:77], v[184:187], v[212:215], v[74:77]
	v_mfma_f32_16x16x32_bf16 v[70:73], v[188:191], v[212:215], v[70:73]
	v_mfma_f32_16x16x32_bf16 v[66:69], v[192:195], v[212:215], v[66:69]
	s_waitcnt lgkmcnt(0)
	s_nop 0
	v_mfma_f32_16x16x32_bf16 v[62:65], v[180:183], v[216:219], v[62:65]
	v_mfma_f32_16x16x32_bf16 v[58:61], v[184:187], v[216:219], v[58:61]
	v_mfma_f32_16x16x32_bf16 v[54:57], v[188:191], v[216:219], v[54:57]
	v_mfma_f32_16x16x32_bf16 v[50:53], v[192:195], v[216:219], v[50:53]
	s_add_i32 s18, 0, 0x10000
	s_waitcnt vmcnt(10)
	v_cvt_pk_bf16_f32 v46, v46, v47
	v_cvt_pk_bf16_f32 v47, v48, v49
	v_cvt_pk_bf16_f32 v48, v42, v43
	v_add_u32_e32 v42, s18, v208
	s_waitcnt vmcnt(8)
	v_cvt_pk_bf16_f32 v38, v38, v39
	v_cvt_pk_bf16_f32 v39, v40, v41
	v_cvt_pk_bf16_f32 v40, v34, v35
	v_add_u32_e32 v34, s18, v205
	s_add_i32 s19, 0, 0x18000
	v_cvt_pk_bf16_f32 v49, v44, v45
	ds_write_b128 v42, v[46:49]
	v_cvt_pk_bf16_f32 v41, v36, v37
	ds_write_b128 v34, v[38:41]
	v_add_u32_e32 v34, s19, v206
	s_waitcnt vmcnt(7)
	ds_write_b128 v34, v[30:33]
	v_add_u32_e32 v30, s19, v207
	s_waitcnt vmcnt(6)
	ds_write_b128 v30, v[26:29]
	ds_read_b128 v[26:29], v210 offset:0x400
	ds_read_b128 v[30:33], v210 offset:0xc00
	ds_read_b128 v[34:37], v210 offset:0x1400
	ds_read_b128 v[38:41], v210 offset:0x1c00
	ds_read_b128 v[42:45], v209 offset:0x400
	ds_read_b128 v[46:49], v209 offset:0xc00
	ds_read_b128 v[180:183], v209 offset:0x1400
	s_nop 0
	s_waitcnt lgkmcnt(2)
	s_nop 0
	v_mfma_f32_16x16x32_bf16 v[174:177], v[26:29], v[42:45], v[174:177]
	v_mfma_f32_16x16x32_bf16 v[170:173], v[30:33], v[42:45], v[170:173]
	v_mfma_f32_16x16x32_bf16 v[166:169], v[34:37], v[42:45], v[166:169]
	v_mfma_f32_16x16x32_bf16 v[42:45], v[38:41], v[42:45], v[162:165]
	ds_read_b128 v[162:165], v209 offset:0x1c00
	s_waitcnt lgkmcnt(2)
	s_nop 0
	v_mfma_f32_16x16x32_bf16 v[158:161], v[26:29], v[46:49], v[158:161]
	v_mfma_f32_16x16x32_bf16 v[154:157], v[30:33], v[46:49], v[154:157]
	v_mfma_f32_16x16x32_bf16 v[150:153], v[34:37], v[46:49], v[150:153]
	v_mfma_f32_16x16x32_bf16 v[46:49], v[38:41], v[46:49], v[146:149]
	ds_read_b128 v[146:149], v209 offset:0x2400
	s_waitcnt lgkmcnt(2)
	s_nop 0
	v_mfma_f32_16x16x32_bf16 v[142:145], v[26:29], v[180:183], v[142:145]
	v_mfma_f32_16x16x32_bf16 v[138:141], v[30:33], v[180:183], v[138:141]
	v_mfma_f32_16x16x32_bf16 v[134:137], v[34:37], v[180:183], v[134:137]
	v_mfma_f32_16x16x32_bf16 v[130:133], v[38:41], v[180:183], v[130:133]
	ds_read_b128 v[180:183], v209 offset:0x2c00
	s_waitcnt lgkmcnt(2)
	s_nop 0
	v_mfma_f32_16x16x32_bf16 v[126:129], v[26:29], v[162:165], v[126:129]
	v_mfma_f32_16x16x32_bf16 v[122:125], v[30:33], v[162:165], v[122:125]
	v_mfma_f32_16x16x32_bf16 v[118:121], v[34:37], v[162:165], v[118:121]
	v_mfma_f32_16x16x32_bf16 v[114:117], v[38:41], v[162:165], v[114:117]
	ds_read_b128 v[162:165], v209 offset:0x3400
	s_waitcnt lgkmcnt(2)
	s_nop 0
	v_mfma_f32_16x16x32_bf16 v[110:113], v[26:29], v[146:149], v[110:113]
	v_mfma_f32_16x16x32_bf16 v[106:109], v[30:33], v[146:149], v[106:109]
	v_mfma_f32_16x16x32_bf16 v[102:105], v[34:37], v[146:149], v[102:105]
	v_mfma_f32_16x16x32_bf16 v[98:101], v[38:41], v[146:149], v[98:101]
	ds_read_b128 v[146:149], v209 offset:0x3c00
	s_waitcnt lgkmcnt(2)
	s_nop 0
	v_mfma_f32_16x16x32_bf16 v[94:97], v[26:29], v[180:183], v[94:97]
	v_mfma_f32_16x16x32_bf16 v[90:93], v[30:33], v[180:183], v[90:93]
	v_mfma_f32_16x16x32_bf16 v[86:89], v[34:37], v[180:183], v[86:89]
	v_mfma_f32_16x16x32_bf16 v[82:85], v[38:41], v[180:183], v[82:85]
	s_waitcnt lgkmcnt(1)
	s_nop 0
	v_mfma_f32_16x16x32_bf16 v[78:81], v[26:29], v[162:165], v[78:81]
	v_mfma_f32_16x16x32_bf16 v[74:77], v[30:33], v[162:165], v[74:77]
	v_mfma_f32_16x16x32_bf16 v[70:73], v[34:37], v[162:165], v[70:73]
	v_mfma_f32_16x16x32_bf16 v[66:69], v[38:41], v[162:165], v[66:69]
	s_waitcnt lgkmcnt(0)
	s_nop 0
	v_mfma_f32_16x16x32_bf16 v[26:29], v[26:29], v[146:149], v[62:65]
	v_mfma_f32_16x16x32_bf16 v[30:33], v[30:33], v[146:149], v[58:61]
	v_mfma_f32_16x16x32_bf16 v[34:37], v[34:37], v[146:149], v[54:57]
	v_mfma_f32_16x16x32_bf16 v[38:41], v[38:41], v[146:149], v[50:53]
	s_waitcnt vmcnt(4)
	v_cvt_pk_bf16_f32 v22, v22, v23
	v_cvt_pk_bf16_f32 v23, v24, v25
	v_cvt_pk_bf16_f32 v24, v6, v7
	v_cvt_pk_bf16_f32 v25, v8, v9
	v_add_u32_e32 v6, s18, v204
	s_waitcnt vmcnt(3)
	v_cvt_pk_bf16_f32 v8, v2, v3
	v_add_u32_e32 v2, s18, v201
	ds_write_b128 v6, v[22:25]
	s_waitcnt vmcnt(2)
	v_cvt_pk_bf16_f32 v6, v10, v11
	v_cvt_pk_bf16_f32 v7, v12, v13
	v_cvt_pk_bf16_f32 v9, v4, v5
	ds_write_b128 v2, v[6:9]
	v_add_u32_e32 v2, s19, v202
	s_waitcnt vmcnt(1)
	ds_write_b128 v2, v[18:21]
	v_add_u32_e32 v2, s19, v203
	s_waitcnt vmcnt(0)
	ds_write_b128 v2, v[14:17]
	s_waitcnt lgkmcnt(0)
	s_barrier
	v_add_u32_e32 v178, 0x10000, v209
	v_add_u32_e32 v196, 0x10000, v210
	ds_read_b128 v[2:5], v196 offset:0
	ds_read_b128 v[6:9], v196 offset:0x800
	ds_read_b128 v[10:13], v196 offset:0x1000
	ds_read_b128 v[14:17], v196 offset:0x1800
	ds_read_b128 v[18:21], v178 offset:0
	s_and_b64 s[16:17], s[16:17], exec
	ds_read_b128 v[22:25], v178 offset:0x800
	ds_read_b128 v[50:53], v178 offset:0x1000
	s_waitcnt lgkmcnt(2)
	s_cselect_b32 s5, s5, s7
	s_cselect_b32 s4, s4, s6
	s_lshl_b32 s6, s3, 10
	v_mfma_f32_16x16x32_bf16 v[54:57], v[2:5], v[18:21], v[174:177]
	s_add_u32 s6, s4, s6
	s_addc_u32 s7, s5, 0
	s_lshl_b32 s3, s3, 9
	v_mfma_f32_16x16x32_bf16 v[58:61], v[6:9], v[18:21], v[170:173]
	s_add_u32 s4, s0, s3
	s_addc_u32 s5, s20, 0
	v_mfma_f32_16x16x32_bf16 v[62:65], v[10:13], v[18:21], v[166:169]
	v_mfma_f32_16x16x32_bf16 v[18:21], v[14:17], v[18:21], v[42:45]
	ds_read_b128 v[42:45], v178 offset:0x1800
	s_waitcnt lgkmcnt(2)
	s_nop 0
	v_mfma_f32_16x16x32_bf16 v[146:149], v[2:5], v[22:25], v[158:161]
	v_mfma_f32_16x16x32_bf16 v[154:157], v[6:9], v[22:25], v[154:157]
	v_mfma_f32_16x16x32_bf16 v[150:153], v[10:13], v[22:25], v[150:153]
	v_mfma_f32_16x16x32_bf16 v[22:25], v[14:17], v[22:25], v[46:49]
	ds_read_b128 v[46:49], v178 offset:0x2000
	s_waitcnt lgkmcnt(2)
	s_nop 0
	v_mfma_f32_16x16x32_bf16 v[142:145], v[2:5], v[50:53], v[142:145]
	v_mfma_f32_16x16x32_bf16 v[138:141], v[6:9], v[50:53], v[138:141]
	v_mfma_f32_16x16x32_bf16 v[134:137], v[10:13], v[50:53], v[134:137]
	v_mfma_f32_16x16x32_bf16 v[50:53], v[14:17], v[50:53], v[130:133]
	ds_read_b128 v[130:133], v178 offset:0x2800
	s_waitcnt lgkmcnt(2)
	s_nop 0
	v_mfma_f32_16x16x32_bf16 v[126:129], v[2:5], v[42:45], v[126:129]
	v_mfma_f32_16x16x32_bf16 v[122:125], v[6:9], v[42:45], v[122:125]
	v_mfma_f32_16x16x32_bf16 v[118:121], v[10:13], v[42:45], v[118:121]
	v_mfma_f32_16x16x32_bf16 v[42:45], v[14:17], v[42:45], v[114:117]
	ds_read_b128 v[114:117], v178 offset:0x3000
	s_waitcnt lgkmcnt(2)
	s_nop 0
	v_mfma_f32_16x16x32_bf16 v[110:113], v[2:5], v[46:49], v[110:113]
	v_mfma_f32_16x16x32_bf16 v[106:109], v[6:9], v[46:49], v[106:109]
	v_mfma_f32_16x16x32_bf16 v[102:105], v[10:13], v[46:49], v[102:105]
	v_mfma_f32_16x16x32_bf16 v[98:101], v[14:17], v[46:49], v[98:101]
	ds_read_b128 v[46:49], v178 offset:0x3800
	s_waitcnt lgkmcnt(2)
	s_nop 0
	v_mfma_f32_16x16x32_bf16 v[158:161], v[2:5], v[130:133], v[94:97]
	v_mfma_f32_16x16x32_bf16 v[162:165], v[6:9], v[130:133], v[90:93]
	v_mfma_f32_16x16x32_bf16 v[166:169], v[10:13], v[130:133], v[86:89]
	v_mfma_f32_16x16x32_bf16 v[130:133], v[14:17], v[130:133], v[82:85]
	s_waitcnt lgkmcnt(1)
	s_nop 0
	v_mfma_f32_16x16x32_bf16 v[66:69], v[14:17], v[114:117], v[66:69]
	v_mfma_f32_16x16x32_bf16 v[170:173], v[2:5], v[114:117], v[78:81]
	v_mfma_f32_16x16x32_bf16 v[174:177], v[6:9], v[114:117], v[74:77]
	v_mfma_f32_16x16x32_bf16 v[180:183], v[10:13], v[114:117], v[70:73]
	s_waitcnt lgkmcnt(0)
	s_nop 0
	v_mfma_f32_16x16x32_bf16 v[2:5], v[2:5], v[46:49], v[26:29]
	v_mfma_f32_16x16x32_bf16 v[114:117], v[6:9], v[46:49], v[30:33]
	v_mfma_f32_16x16x32_bf16 v[34:37], v[10:13], v[46:49], v[34:37]
	v_mfma_f32_16x16x32_bf16 v[184:187], v[14:17], v[46:49], v[38:41]
	ds_read_b128 v[188:191], v196 offset:0x400
	ds_read_b128 v[192:195], v196 offset:0xc00
	ds_read_b128 v[202:205], v196 offset:0x1400
	ds_read_b128 v[206:209], v196 offset:0x1c00
	ds_read_b128 v[6:9], v178 offset:0x400
	ds_read_b128 v[10:13], v178 offset:0xc00
	ds_read_b128 v[14:17], v178 offset:0x1400
	s_nop 0
	s_waitcnt lgkmcnt(2)
	s_nop 0
	v_mfma_f32_16x16x32_bf16 v[94:97], v[192:195], v[6:9], v[58:61]
	v_mfma_f32_16x16x32_bf16 v[62:65], v[202:205], v[6:9], v[62:65]
	v_mfma_f32_16x16x32_bf16 v[30:33], v[206:209], v[6:9], v[18:21]
	v_mfma_f32_16x16x32_bf16 v[210:213], v[188:191], v[6:9], v[54:57]
	ds_read_b128 v[6:9], v178 offset:0x1c00
	s_waitcnt lgkmcnt(2)
	s_nop 0
	v_mfma_f32_16x16x32_bf16 v[90:93], v[192:195], v[10:13], v[154:157]
	v_mfma_f32_16x16x32_bf16 v[58:61], v[202:205], v[10:13], v[150:153]
	v_mfma_f32_16x16x32_bf16 v[26:29], v[206:209], v[10:13], v[22:25]
	v_mfma_f32_16x16x32_bf16 v[146:149], v[188:191], v[10:13], v[146:149]
	ds_read_b128 v[10:13], v178 offset:0x2400
	s_waitcnt lgkmcnt(2)
	s_nop 0
	v_mfma_f32_16x16x32_bf16 v[86:89], v[192:195], v[14:17], v[138:141]
	v_mfma_f32_16x16x32_bf16 v[54:57], v[202:205], v[14:17], v[134:137]
	v_mfma_f32_16x16x32_bf16 v[22:25], v[206:209], v[14:17], v[50:53]
	v_mfma_f32_16x16x32_bf16 v[142:145], v[188:191], v[14:17], v[142:145]
	ds_read_b128 v[38:41], v178 offset:0x2c00
	s_waitcnt lgkmcnt(2)
	s_nop 0
	v_mfma_f32_16x16x32_bf16 v[126:129], v[188:191], v[6:9], v[126:129]
	v_mfma_f32_16x16x32_bf16 v[82:85], v[192:195], v[6:9], v[122:125]
	v_mfma_f32_16x16x32_bf16 v[50:53], v[202:205], v[6:9], v[118:121]
	v_mfma_f32_16x16x32_bf16 v[18:21], v[206:209], v[6:9], v[42:45]
	ds_read_b128 v[6:9], v178 offset:0x3400
	s_waitcnt lgkmcnt(2)
	s_nop 0
	v_mfma_f32_16x16x32_bf16 v[110:113], v[188:191], v[10:13], v[110:113]
	v_mfma_f32_16x16x32_bf16 v[78:81], v[192:195], v[10:13], v[106:109]
	v_mfma_f32_16x16x32_bf16 v[46:49], v[202:205], v[10:13], v[102:105]
	v_mfma_f32_16x16x32_bf16 v[14:17], v[206:209], v[10:13], v[98:101]
	ds_read_b128 v[98:101], v178 offset:0x3c00
	s_waitcnt lgkmcnt(2)
	s_nop 0
	v_mfma_f32_16x16x32_bf16 v[106:109], v[188:191], v[38:41], v[158:161]
	v_mfma_f32_16x16x32_bf16 v[74:77], v[192:195], v[38:41], v[162:165]
	v_mfma_f32_16x16x32_bf16 v[42:45], v[202:205], v[38:41], v[166:169]
	v_mfma_f32_16x16x32_bf16 v[10:13], v[206:209], v[38:41], v[130:133]
	s_waitcnt lgkmcnt(1)
	s_nop 0
	v_mfma_f32_16x16x32_bf16 v[118:121], v[188:191], v[6:9], v[170:173]
	v_mfma_f32_16x16x32_bf16 v[70:73], v[192:195], v[6:9], v[174:177]
	v_mfma_f32_16x16x32_bf16 v[38:41], v[202:205], v[6:9], v[180:183]
	v_mfma_f32_16x16x32_bf16 v[6:9], v[206:209], v[6:9], v[66:69]
	s_waitcnt lgkmcnt(0)
	s_nop 0
	v_mfma_f32_16x16x32_bf16 v[122:125], v[188:191], v[98:101], v[2:5]
	v_mfma_f32_16x16x32_bf16 v[66:69], v[192:195], v[98:101], v[114:117]
	v_mfma_f32_16x16x32_bf16 v[34:37], v[202:205], v[98:101], v[34:37]
	v_mfma_f32_16x16x32_bf16 v[2:5], v[206:209], v[98:101], v[184:187]
	v_lshrrev_b32_e32 v98, 2, v199
	v_and_b32_e32 v98, 12, v98
	v_lshl_or_b32 v104, v200, 6, v98
	v_lshlrev_b32_e32 v105, 2, v104
	s_waitcnt lgkmcnt(0)
	s_barrier
	global_load_dwordx4 v[114:117], v105, s[6:7]
	v_lshrrev_b32_e32 v98, 1, v199
	v_lshlrev_b32_e32 v99, 16, v198
	v_lshlrev_b32_e32 v100, 9, v179
	v_and_b32_e32 v102, 8, v98
	v_lshrrev_b32_e32 v98, 3, v104
	v_add3_u32 v103, 0, v99, v100
	v_xor_b32_e32 v130, v98, v179
	v_bitop3_b32 v131, v98, v179, 16 bitop3:0x1e
	global_load_dwordx4 v[98:101], v105, s[6:7] offset:64
	v_lshlrev_b32_e32 v130, 4, v130
	v_lshlrev_b32_e32 v131, 4, v131
	v_add3_u32 v130, v103, v130, v102
	v_add3_u32 v131, v103, v131, v102
	s_movk_i32 s0, 0x200
	s_waitcnt vmcnt(1)
	v_add_f32_e32 v132, v210, v114
	v_add_f32_e32 v133, v211, v115
	v_add_f32_e32 v134, v212, v116
	v_add_f32_e32 v135, v213, v117
	v_add_f32_e32 v140, v142, v114
	v_add_f32_e32 v141, v143, v115
	v_add_f32_e32 v142, v144, v116
	v_add_f32_e32 v143, v145, v117
	v_add_f32_e32 v110, v110, v114
	v_add_f32_e32 v111, v111, v115
	v_add_f32_e32 v106, v106, v114
	v_add_f32_e32 v107, v107, v115
	v_add_f32_e32 v136, v146, v114
	v_add_f32_e32 v137, v147, v115
	v_add_f32_e32 v138, v148, v116
	v_add_f32_e32 v139, v149, v117
	v_add_f32_e32 v126, v126, v114
	v_add_f32_e32 v127, v127, v115
	v_add_f32_e32 v128, v128, v116
	v_add_f32_e32 v129, v129, v117
	v_add_f32_e32 v112, v112, v116
	v_add_f32_e32 v113, v113, v117
	v_add_f32_e32 v108, v108, v116
	v_add_f32_e32 v109, v109, v117
	v_max_f32_e32 v132, 0, v132
	v_max_f32_e32 v133, 0, v133
	v_max_f32_e32 v134, 0, v134
	v_max_f32_e32 v135, 0, v135
	v_max_f32_e32 v140, 0, v140
	v_max_f32_e32 v141, 0, v141
	v_max_f32_e32 v142, 0, v142
	v_max_f32_e32 v143, 0, v143
	v_max_f32_e32 v144, 0, v110
	v_max_f32_e32 v145, 0, v111
	v_max_f32_e32 v148, 0, v106
	v_max_f32_e32 v149, 0, v107
	v_cvt_pk_bf16_f32 v106, v132, v133
	v_cvt_pk_bf16_f32 v107, v134, v135
	v_cvt_pk_bf16_f32 v110, v140, v141
	v_cvt_pk_bf16_f32 v111, v142, v143
	v_add_f32_e32 v118, v118, v114
	v_add_f32_e32 v119, v119, v115
	v_max_f32_e32 v136, 0, v136
	v_max_f32_e32 v137, 0, v137
	v_max_f32_e32 v138, 0, v138
	v_max_f32_e32 v139, 0, v139
	v_max_f32_e32 v126, 0, v126
	v_max_f32_e32 v127, 0, v127
	v_max_f32_e32 v128, 0, v128
	v_max_f32_e32 v129, 0, v129
	v_max_f32_e32 v146, 0, v112
	v_max_f32_e32 v147, 0, v113
	v_max_f32_e32 v150, 0, v108
	v_max_f32_e32 v151, 0, v109
	v_cvt_pk_bf16_f32 v108, v136, v137
	v_cvt_pk_bf16_f32 v109, v138, v139
	v_cvt_pk_bf16_f32 v112, v126, v127
	v_cvt_pk_bf16_f32 v113, v128, v129
	ds_write2st64_b64 v130, v[106:107], v[110:111] offset1:32
	ds_write2st64_b64 v131, v[108:109], v[112:113] offset0:16 offset1:48
	v_add_f32_e32 v106, v121, v117
	v_add_f32_e32 v120, v120, v116
	v_max_f32_e32 v152, 0, v118
	v_max_f32_e32 v153, 0, v119
	v_max_f32_e32 v107, 0, v106
	v_cvt_pk_bf16_f32 v106, v152, v153
	v_max_f32_e32 v120, 0, v120
	v_cvt_pk_bf16_f32 v118, v144, v145
	v_cvt_pk_bf16_f32 v119, v146, v147
	v_cvt_pk_bf16_f32 v107, v120, v107
	ds_write2st64_b64 v130, v[118:119], v[106:107] offset0:64 offset1:96
	v_add_f32_e32 v106, v122, v114
	v_max_f32_e32 v106, 0, v106
	v_add_f32_e32 v107, v123, v115
	v_max_f32_e32 v107, 0, v107
	v_add_f32_e32 v108, v124, v116
	v_add_f32_e32 v109, v125, v117
	v_cvt_pk_bf16_f32 v106, v106, v107
	v_cvt_pk_bf16_f32 v126, v148, v149
	v_cvt_pk_bf16_f32 v127, v150, v151
	v_max_f32_e32 v108, 0, v108
	v_max_f32_e32 v109, 0, v109
	v_cvt_pk_bf16_f32 v107, v108, v109
	ds_write2st64_b64 v131, v[126:127], v[106:107] offset0:80 offset1:112
	v_or_b32_e32 v106, 16, v104
	s_waitcnt vmcnt(0)
	v_add_f32_e32 v94, v94, v98
	v_add_f32_e32 v95, v95, v99
	v_add_f32_e32 v96, v96, v100
	v_lshrrev_b32_e32 v106, 3, v106
	v_max_f32_e32 v94, 0, v94
	v_max_f32_e32 v95, 0, v95
	v_max_f32_e32 v96, 0, v96
	v_add_f32_e32 v97, v97, v101
	v_max_f32_e32 v97, 0, v97
	v_cvt_pk_bf16_f32 v94, v94, v95
	v_cvt_pk_bf16_f32 v95, v96, v97
	v_xor_b32_e32 v96, v106, v179
	v_lshlrev_b32_e32 v96, 4, v96
	v_add3_u32 v107, v103, v96, v102
	v_add_f32_e32 v90, v90, v98
	v_add_f32_e32 v91, v91, v99
	v_add_f32_e32 v92, v92, v100
	ds_write_b64 v107, v[94:95]
	v_max_f32_e32 v90, 0, v90
	v_max_f32_e32 v91, 0, v91
	global_load_dwordx4 v[94:97], v105, s[6:7] offset:128
	v_max_f32_e32 v92, 0, v92
	v_add_f32_e32 v93, v93, v101
	v_max_f32_e32 v93, 0, v93
	v_cvt_pk_bf16_f32 v90, v90, v91
	v_cvt_pk_bf16_f32 v91, v92, v93
	v_bitop3_b32 v92, v106, v179, 16 bitop3:0x1e
	v_add_f32_e32 v66, v66, v98
	v_lshlrev_b32_e32 v92, 4, v92
	v_add_f32_e32 v86, v86, v98
	v_add_f32_e32 v87, v87, v99
	v_add_f32_e32 v82, v82, v98
	v_add_f32_e32 v83, v83, v99
	v_add_f32_e32 v78, v78, v98
	v_add_f32_e32 v79, v79, v99
	v_add_f32_e32 v74, v74, v98
	v_add_f32_e32 v75, v75, v99
	v_add_f32_e32 v70, v70, v98
	v_add_f32_e32 v71, v71, v99
	v_max_f32_e32 v66, 0, v66
	v_add_f32_e32 v67, v67, v99
	v_add3_u32 v92, v103, v92, v102
	v_max_f32_e32 v86, 0, v86
	v_max_f32_e32 v87, 0, v87
	v_add_f32_e32 v88, v88, v100
	v_add_f32_e32 v89, v89, v101
	v_max_f32_e32 v82, 0, v82
	v_max_f32_e32 v83, 0, v83
	v_add_f32_e32 v84, v84, v100
	v_add_f32_e32 v85, v85, v101
	v_max_f32_e32 v78, 0, v78
	v_max_f32_e32 v79, 0, v79
	v_add_f32_e32 v80, v80, v100
	v_add_f32_e32 v81, v81, v101
	v_max_f32_e32 v74, 0, v74
	v_max_f32_e32 v75, 0, v75
	v_add_f32_e32 v76, v76, v100
	v_add_f32_e32 v77, v77, v101
	v_max_f32_e32 v70, 0, v70
	v_max_f32_e32 v71, 0, v71
	v_add_f32_e32 v72, v72, v100
	v_add_f32_e32 v73, v73, v101
	v_max_f32_e32 v67, 0, v67
	v_add_f32_e32 v68, v68, v100
	v_add_f32_e32 v69, v69, v101
	v_cvt_pk_bf16_f32 v66, v66, v67
	ds_write_b64 v92, v[90:91] offset:8192
	v_max_f32_e32 v88, 0, v88
	v_max_f32_e32 v89, 0, v89
	v_cvt_pk_bf16_f32 v86, v86, v87
	v_cvt_pk_bf16_f32 v87, v88, v89
	ds_write_b64 v107, v[86:87] offset:16384
	v_max_f32_e32 v84, 0, v84
	v_max_f32_e32 v85, 0, v85
	v_cvt_pk_bf16_f32 v82, v82, v83
	v_cvt_pk_bf16_f32 v83, v84, v85
	ds_write_b64 v92, v[82:83] offset:24576
	v_max_f32_e32 v80, 0, v80
	v_max_f32_e32 v81, 0, v81
	v_cvt_pk_bf16_f32 v78, v78, v79
	v_cvt_pk_bf16_f32 v79, v80, v81
	ds_write_b64 v107, v[78:79] offset:32768
	v_max_f32_e32 v76, 0, v76
	v_max_f32_e32 v77, 0, v77
	v_cvt_pk_bf16_f32 v74, v74, v75
	v_cvt_pk_bf16_f32 v75, v76, v77
	ds_write_b64 v92, v[74:75] offset:40960
	v_max_f32_e32 v72, 0, v72
	v_max_f32_e32 v73, 0, v73
	v_cvt_pk_bf16_f32 v70, v70, v71
	v_cvt_pk_bf16_f32 v71, v72, v73
	ds_write_b64 v107, v[70:71] offset:49152
	v_max_f32_e32 v68, 0, v68
	v_max_f32_e32 v69, 0, v69
	v_cvt_pk_bf16_f32 v67, v68, v69
	ds_write_b64 v92, v[66:67] offset:57344
	v_or_b32_e32 v66, 32, v104
	v_lshrrev_b32_e32 v70, 3, v66
	global_load_dwordx4 v[66:69], v105, s[6:7] offset:192
	s_waitcnt vmcnt(1)
	v_add_f32_e32 v62, v62, v94
	v_add_f32_e32 v63, v63, v95
	v_add_f32_e32 v64, v64, v96
	v_add_f32_e32 v58, v58, v94
	v_add_f32_e32 v59, v59, v95
	v_add_f32_e32 v60, v60, v96
	v_max_f32_e32 v62, 0, v62
	v_max_f32_e32 v63, 0, v63
	v_max_f32_e32 v64, 0, v64
	v_add_f32_e32 v65, v65, v97
	v_max_f32_e32 v58, 0, v58
	v_max_f32_e32 v59, 0, v59
	v_max_f32_e32 v60, 0, v60
	v_add_f32_e32 v61, v61, v97
	v_max_f32_e32 v65, 0, v65
	v_cvt_pk_bf16_f32 v62, v62, v63
	v_cvt_pk_bf16_f32 v63, v64, v65
	v_xor_b32_e32 v64, v70, v179
	v_max_f32_e32 v61, 0, v61
	v_cvt_pk_bf16_f32 v58, v58, v59
	v_cvt_pk_bf16_f32 v59, v60, v61
	v_bitop3_b32 v60, v70, v179, 16 bitop3:0x1e
	v_add_f32_e32 v34, v34, v94
	v_lshlrev_b32_e32 v64, 4, v64
	v_lshlrev_b32_e32 v60, 4, v60
	v_add_f32_e32 v54, v54, v94
	v_add_f32_e32 v55, v55, v95
	v_add_f32_e32 v50, v50, v94
	v_add_f32_e32 v51, v51, v95
	v_add_f32_e32 v46, v46, v94
	v_add_f32_e32 v47, v47, v95
	v_add_f32_e32 v42, v42, v94
	v_add_f32_e32 v43, v43, v95
	v_add_f32_e32 v38, v38, v94
	v_add_f32_e32 v39, v39, v95
	v_max_f32_e32 v34, 0, v34
	v_add_f32_e32 v35, v35, v95
	v_add3_u32 v64, v103, v64, v102
	v_add3_u32 v60, v103, v60, v102
	v_max_f32_e32 v54, 0, v54
	v_max_f32_e32 v55, 0, v55
	v_add_f32_e32 v56, v56, v96
	v_add_f32_e32 v57, v57, v97
	v_max_f32_e32 v50, 0, v50
	v_max_f32_e32 v51, 0, v51
	v_add_f32_e32 v52, v52, v96
	v_add_f32_e32 v53, v53, v97
	v_max_f32_e32 v46, 0, v46
	v_max_f32_e32 v47, 0, v47
	v_add_f32_e32 v48, v48, v96
	v_add_f32_e32 v49, v49, v97
	v_max_f32_e32 v42, 0, v42
	v_max_f32_e32 v43, 0, v43
	v_add_f32_e32 v44, v44, v96
	v_add_f32_e32 v45, v45, v97
	v_max_f32_e32 v38, 0, v38
	v_max_f32_e32 v39, 0, v39
	v_add_f32_e32 v40, v40, v96
	v_add_f32_e32 v41, v41, v97
	v_max_f32_e32 v35, 0, v35
	v_add_f32_e32 v36, v36, v96
	v_add_f32_e32 v37, v37, v97
	v_cvt_pk_bf16_f32 v34, v34, v35
	ds_write_b64 v64, v[62:63]
	ds_write_b64 v60, v[58:59] offset:8192
	v_max_f32_e32 v56, 0, v56
	v_max_f32_e32 v57, 0, v57
	v_cvt_pk_bf16_f32 v54, v54, v55
	v_cvt_pk_bf16_f32 v55, v56, v57
	ds_write_b64 v64, v[54:55] offset:16384
	v_max_f32_e32 v52, 0, v52
	v_max_f32_e32 v53, 0, v53
	v_cvt_pk_bf16_f32 v50, v50, v51
	v_cvt_pk_bf16_f32 v51, v52, v53
	ds_write_b64 v60, v[50:51] offset:24576
	v_max_f32_e32 v48, 0, v48
	v_max_f32_e32 v49, 0, v49
	v_cvt_pk_bf16_f32 v46, v46, v47
	v_cvt_pk_bf16_f32 v47, v48, v49
	ds_write_b64 v64, v[46:47] offset:32768
	v_max_f32_e32 v44, 0, v44
	v_max_f32_e32 v45, 0, v45
	v_cvt_pk_bf16_f32 v42, v42, v43
	v_cvt_pk_bf16_f32 v43, v44, v45
	ds_write_b64 v60, v[42:43] offset:40960
	v_max_f32_e32 v40, 0, v40
	v_max_f32_e32 v41, 0, v41
	v_cvt_pk_bf16_f32 v38, v38, v39
	v_cvt_pk_bf16_f32 v39, v40, v41
	ds_write_b64 v64, v[38:39] offset:49152
	v_max_f32_e32 v36, 0, v36
	v_max_f32_e32 v37, 0, v37
	v_cvt_pk_bf16_f32 v35, v36, v37
	ds_write_b64 v60, v[34:35] offset:57344
	v_or_b32_e32 v34, 48, v104
	s_waitcnt vmcnt(0)
	v_add_f32_e32 v30, v30, v66
	v_add_f32_e32 v31, v31, v67
	v_add_f32_e32 v32, v32, v68
	v_add_f32_e32 v26, v26, v66
	v_add_f32_e32 v27, v27, v67
	v_add_f32_e32 v28, v28, v68
	v_lshrrev_b32_e32 v34, 3, v34
	v_max_f32_e32 v30, 0, v30
	v_max_f32_e32 v31, 0, v31
	v_max_f32_e32 v32, 0, v32
	v_add_f32_e32 v33, v33, v69
	v_max_f32_e32 v26, 0, v26
	v_max_f32_e32 v27, 0, v27
	v_max_f32_e32 v28, 0, v28
	v_add_f32_e32 v29, v29, v69
	v_max_f32_e32 v33, 0, v33
	v_cvt_pk_bf16_f32 v30, v30, v31
	v_cvt_pk_bf16_f32 v31, v32, v33
	v_xor_b32_e32 v32, v34, v179
	v_max_f32_e32 v29, 0, v29
	v_cvt_pk_bf16_f32 v26, v26, v27
	v_cvt_pk_bf16_f32 v27, v28, v29
	v_bitop3_b32 v28, v34, v179, 16 bitop3:0x1e
	v_add_f32_e32 v2, v2, v66
	v_lshlrev_b32_e32 v32, 4, v32
	v_lshlrev_b32_e32 v28, 4, v28
	v_add_f32_e32 v22, v22, v66
	v_add_f32_e32 v23, v23, v67
	v_add_f32_e32 v18, v18, v66
	v_add_f32_e32 v19, v19, v67
	v_add_f32_e32 v14, v14, v66
	v_add_f32_e32 v15, v15, v67
	v_add_f32_e32 v10, v10, v66
	v_add_f32_e32 v11, v11, v67
	v_add_f32_e32 v6, v6, v66
	v_add_f32_e32 v7, v7, v67
	v_max_f32_e32 v2, 0, v2
	v_add_f32_e32 v3, v3, v67
	v_add3_u32 v32, v103, v32, v102
	v_add3_u32 v28, v103, v28, v102
	v_max_f32_e32 v22, 0, v22
	v_max_f32_e32 v23, 0, v23
	v_add_f32_e32 v24, v24, v68
	v_add_f32_e32 v25, v25, v69
	v_max_f32_e32 v18, 0, v18
	v_max_f32_e32 v19, 0, v19
	v_add_f32_e32 v20, v20, v68
	v_add_f32_e32 v21, v21, v69
	v_max_f32_e32 v14, 0, v14
	v_max_f32_e32 v15, 0, v15
	v_add_f32_e32 v16, v16, v68
	v_add_f32_e32 v17, v17, v69
	v_max_f32_e32 v10, 0, v10
	v_max_f32_e32 v11, 0, v11
	v_add_f32_e32 v12, v12, v68
	v_add_f32_e32 v13, v13, v69
	v_max_f32_e32 v6, 0, v6
	v_max_f32_e32 v7, 0, v7
	v_add_f32_e32 v8, v8, v68
	v_add_f32_e32 v9, v9, v69
	v_max_f32_e32 v3, 0, v3
	v_add_f32_e32 v4, v4, v68
	v_add_f32_e32 v5, v5, v69
	v_cvt_pk_bf16_f32 v2, v2, v3
	ds_write_b64 v32, v[30:31]
	ds_write_b64 v28, v[26:27] offset:8192
	v_max_f32_e32 v24, 0, v24
	v_max_f32_e32 v25, 0, v25
	v_cvt_pk_bf16_f32 v22, v22, v23
	v_cvt_pk_bf16_f32 v23, v24, v25
	ds_write_b64 v32, v[22:23] offset:16384
	v_max_f32_e32 v20, 0, v20
	v_max_f32_e32 v21, 0, v21
	v_cvt_pk_bf16_f32 v18, v18, v19
	v_cvt_pk_bf16_f32 v19, v20, v21
	ds_write_b64 v28, v[18:19] offset:24576
	v_max_f32_e32 v16, 0, v16
	v_max_f32_e32 v17, 0, v17
	v_cvt_pk_bf16_f32 v14, v14, v15
	v_cvt_pk_bf16_f32 v15, v16, v17
	ds_write_b64 v32, v[14:15] offset:32768
	v_max_f32_e32 v12, 0, v12
	v_max_f32_e32 v13, 0, v13
	v_cvt_pk_bf16_f32 v10, v10, v11
	v_cvt_pk_bf16_f32 v11, v12, v13
	ds_write_b64 v28, v[10:11] offset:40960
	v_max_f32_e32 v8, 0, v8
	v_max_f32_e32 v9, 0, v9
	v_cvt_pk_bf16_f32 v6, v6, v7
	v_cvt_pk_bf16_f32 v7, v8, v9
	ds_write_b64 v32, v[6:7] offset:49152
	v_max_f32_e32 v4, 0, v4
	v_max_f32_e32 v5, 0, v5
	v_cvt_pk_bf16_f32 v3, v4, v5
	ds_write_b64 v28, v[2:3] offset:57344
	v_and_b32_e32 v2, 0x1f0, v1
	v_lshrrev_b32_e32 v1, 5, v0
	v_xor_b32_e32 v4, v1, v0
	v_mov_b32_e32 v3, 0
	v_lshlrev_b32_e32 v4, 4, v4
	v_lshl_add_u64 v[12:13], s[4:5], 0, v[2:3]
	v_lshlrev_b32_e32 v2, 9, v1
	v_and_b32_e32 v16, 0x1f0, v4
	v_add3_u32 v2, 0, v2, v16
	s_waitcnt lgkmcnt(0)
	s_barrier
	ds_read_b128 v[4:7], v2
	v_lshlrev_b32_e32 v2, 11, v1
	v_lshl_add_u64 v[14:15], v[12:13], 0, v[2:3]
	v_or_b32_e32 v2, 0x200, v0
	v_lshrrev_b32_e32 v2, 5, v2
	v_xor_b32_e32 v9, v2, v0
	v_lshlrev_b32_e32 v9, 4, v9
	v_lshlrev_b32_e32 v8, 9, v2
	v_and_b32_e32 v9, 0x1f0, v9
	v_add3_u32 v8, 0, v8, v9
	ds_read_b128 v[8:11], v8
	v_lshlrev_b32_e32 v2, 11, v2
	s_waitcnt lgkmcnt(1)
	global_store_dwordx4 v[14:15], v[4:7], off sc1
	s_nop 1
	v_lshl_add_u64 v[4:5], v[12:13], 0, v[2:3]
	s_waitcnt lgkmcnt(0)
	global_store_dwordx4 v[4:5], v[8:11], off sc1
	v_or_b32_e32 v2, 32, v1
	v_lshlrev_b32_e32 v4, 9, v2
	v_or_b32_e32 v8, 0x600, v0
	v_lshrrev_b32_e32 v17, 5, v8
	v_xor_b32_e32 v9, v17, v0
	v_lshlrev_b32_e32 v9, 4, v9
	v_add3_u32 v4, 0, v4, v16
	v_lshlrev_b32_e32 v8, 9, v17
	v_and_b32_e32 v9, 0x1f0, v9
	ds_read_b128 v[4:7], v4
	v_add3_u32 v8, 0, v8, v9
	ds_read_b128 v[8:11], v8
	v_lshlrev_b32_e32 v2, 11, v2
	v_lshl_add_u64 v[14:15], v[12:13], 0, v[2:3]
	v_lshlrev_b32_e32 v2, 11, v17
	s_waitcnt lgkmcnt(1)
	global_store_dwordx4 v[14:15], v[4:7], off sc1
	s_nop 1
	v_lshl_add_u64 v[4:5], v[12:13], 0, v[2:3]
	s_waitcnt lgkmcnt(0)
	global_store_dwordx4 v[4:5], v[8:11], off sc1
	v_or_b32_e32 v2, 64, v1
	v_lshlrev_b32_e32 v4, 9, v2
	v_or_b32_e32 v8, 0xa00, v0
	v_lshrrev_b32_e32 v17, 5, v8
	v_xor_b32_e32 v9, v17, v0
	v_lshlrev_b32_e32 v9, 4, v9
	v_add3_u32 v4, 0, v4, v16
	v_lshlrev_b32_e32 v8, 9, v17
	v_and_b32_e32 v9, 0x1f0, v9
	ds_read_b128 v[4:7], v4
	v_add3_u32 v8, 0, v8, v9
	ds_read_b128 v[8:11], v8
	v_lshlrev_b32_e32 v2, 11, v2
	v_lshl_add_u64 v[14:15], v[12:13], 0, v[2:3]
	v_lshlrev_b32_e32 v2, 11, v17
	s_waitcnt lgkmcnt(1)
	global_store_dwordx4 v[14:15], v[4:7], off sc1
	s_nop 1
	v_lshl_add_u64 v[4:5], v[12:13], 0, v[2:3]
	s_waitcnt lgkmcnt(0)
	global_store_dwordx4 v[4:5], v[8:11], off sc1
	v_or_b32_e32 v2, 0x60, v1
	v_lshlrev_b32_e32 v4, 9, v2
	v_or_b32_e32 v8, 0xe00, v0
	v_lshrrev_b32_e32 v17, 5, v8
	v_xor_b32_e32 v9, v17, v0
	v_lshlrev_b32_e32 v9, 4, v9
	v_add3_u32 v4, 0, v4, v16
	v_lshlrev_b32_e32 v8, 9, v17
	v_and_b32_e32 v9, 0x1f0, v9
	ds_read_b128 v[4:7], v4
	v_add3_u32 v8, 0, v8, v9
	ds_read_b128 v[8:11], v8
	v_lshlrev_b32_e32 v2, 11, v2
	v_lshl_add_u64 v[14:15], v[12:13], 0, v[2:3]
	v_lshlrev_b32_e32 v2, 11, v17
	s_waitcnt lgkmcnt(1)
	global_store_dwordx4 v[14:15], v[4:7], off sc1
	s_nop 1
	v_lshl_add_u64 v[4:5], v[12:13], 0, v[2:3]
	s_waitcnt lgkmcnt(0)
	global_store_dwordx4 v[4:5], v[8:11], off sc1
	v_or_b32_e32 v2, 0x80, v1
	v_lshlrev_b32_e32 v4, 9, v2
	v_or_b32_e32 v8, 0x1200, v0
	v_lshrrev_b32_e32 v17, 5, v8
	v_xor_b32_e32 v9, v17, v0
	v_lshlrev_b32_e32 v9, 4, v9
	v_add3_u32 v4, 0, v4, v16
	v_lshlrev_b32_e32 v8, 9, v17
	v_and_b32_e32 v9, 0x1f0, v9
	ds_read_b128 v[4:7], v4
	v_add3_u32 v8, 0, v8, v9
	ds_read_b128 v[8:11], v8
	v_lshlrev_b32_e32 v2, 11, v2
	v_lshl_add_u64 v[14:15], v[12:13], 0, v[2:3]
	v_lshlrev_b32_e32 v2, 11, v17
	s_waitcnt lgkmcnt(1)
	global_store_dwordx4 v[14:15], v[4:7], off sc1
	s_nop 1
	v_lshl_add_u64 v[4:5], v[12:13], 0, v[2:3]
	s_waitcnt lgkmcnt(0)
	global_store_dwordx4 v[4:5], v[8:11], off sc1
	v_or_b32_e32 v2, 0xa0, v1
	v_lshlrev_b32_e32 v4, 9, v2
	v_or_b32_e32 v8, 0x1600, v0
	v_lshrrev_b32_e32 v17, 5, v8
	v_xor_b32_e32 v9, v17, v0
	v_lshlrev_b32_e32 v9, 4, v9
	v_add3_u32 v4, 0, v4, v16
	v_lshlrev_b32_e32 v8, 9, v17
	v_and_b32_e32 v9, 0x1f0, v9
	ds_read_b128 v[4:7], v4
	v_add3_u32 v8, 0, v8, v9
	ds_read_b128 v[8:11], v8
	v_lshlrev_b32_e32 v2, 11, v2
	v_lshl_add_u64 v[14:15], v[12:13], 0, v[2:3]
	v_lshlrev_b32_e32 v2, 11, v17
	s_waitcnt lgkmcnt(1)
	global_store_dwordx4 v[14:15], v[4:7], off sc1
	s_nop 1
	v_lshl_add_u64 v[4:5], v[12:13], 0, v[2:3]
	s_waitcnt lgkmcnt(0)
	global_store_dwordx4 v[4:5], v[8:11], off sc1
	v_or_b32_e32 v2, 0xc0, v1
	v_lshlrev_b32_e32 v4, 9, v2
	v_or_b32_e32 v8, 0x1a00, v0
	v_lshrrev_b32_e32 v17, 5, v8
	v_xor_b32_e32 v9, v17, v0
	v_add3_u32 v4, 0, v4, v16
	v_lshlrev_b32_e32 v9, 4, v9
	ds_read_b128 v[4:7], v4
	v_lshlrev_b32_e32 v8, 9, v17
	v_and_b32_e32 v9, 0x1f0, v9
	v_add3_u32 v8, 0, v8, v9
	ds_read_b128 v[8:11], v8
	v_lshlrev_b32_e32 v2, 11, v2
	v_lshl_add_u64 v[14:15], v[12:13], 0, v[2:3]
	v_lshlrev_b32_e32 v2, 11, v17
	v_or_b32_e32 v1, 0xe0, v1
	s_waitcnt lgkmcnt(1)
	global_store_dwordx4 v[14:15], v[4:7], off sc1
	s_nop 1
	v_lshl_add_u64 v[4:5], v[12:13], 0, v[2:3]
	v_lshlrev_b32_e32 v2, 9, v1
	v_add3_u32 v2, 0, v2, v16
	s_waitcnt lgkmcnt(0)
	global_store_dwordx4 v[4:5], v[8:11], off sc1
	ds_read_b128 v[4:7], v2
	v_lshlrev_b32_e32 v2, 11, v1
	v_or_b32_e32 v1, 0x1e00, v0
	v_lshrrev_b32_e32 v1, 5, v1
	v_xor_b32_e32 v9, v1, v0
	v_lshlrev_b32_e32 v9, 4, v9
	v_lshlrev_b32_e32 v8, 9, v1
	v_and_b32_e32 v9, 0x1f0, v9
	v_add3_u32 v8, 0, v8, v9
	ds_read_b128 v[8:11], v8
	v_lshl_add_u64 v[14:15], v[12:13], 0, v[2:3]
	v_lshlrev_b32_e32 v2, 11, v1
	s_waitcnt lgkmcnt(1)
	global_store_dwordx4 v[14:15], v[4:7], off sc1
	s_nop 1
	v_lshl_add_u64 v[4:5], v[12:13], 0, v[2:3]
	s_waitcnt lgkmcnt(0)
	global_store_dwordx4 v[4:5], v[8:11], off sc1
	s_waitcnt lgkmcnt(0)
	s_barrier
	s_lshl_b32 s3, s2, 3
	s_and_b32 s3, s3, 56
	s_ashr_i32 s17, s2, 5
	s_add_i32 s20, s3, s17
	s_ashr_i32 s21, s20, 31
	s_bfe_u32 s16, s2, 0x20003
	s_lshl_b64 s[4:5], s[20:21], 17
	s_lshl_b64 s[6:7], s[20:21], 19
	s_add_u32 s6, s12, s6
	s_addc_u32 s7, s13, s7
	s_lshl_b32 s3, s16, 19
	s_add_u32 s3, s14, s3
	v_ashrrev_i32_e32 v2, 6, v0
	v_lshlrev_b32_e32 v1, 4, v0
	s_addc_u32 s13, s15, 0
	v_lshlrev_b32_e32 v4, 9, v2
	v_and_b32_e32 v5, 0x1f0, v1
	s_add_u32 s12, s3, 0x400000
	v_and_or_b32 v32, v4, s0, v5
	v_lshlrev_b32_e32 v4, 5, v2
	v_and_b32_e32 v5, 48, v1
	s_addc_u32 s13, s13, 0
	v_bitop3_b32 v4, v4, v5, 32 bitop3:0x6c
	s_and_b32 s15, s2, 8
	s_add_i32 s3, s20, 3
	v_bfe_u32 v31, v0, 5, 1
	v_lshrrev_b32_e32 v34, 1, v4
	v_add_u32_e32 v4, s15, v2
	s_mov_b32 s20, 0x3ffffe
	v_and_or_b32 v30, v4, s20, v31
	v_bfe_i32 v5, v30, 0, 22
	v_bfe_u32 v4, v30, 21, 1
	v_add_u32_e32 v6, v5, v4
	v_lshlrev_b32_e32 v4, 3, v6
	v_and_b32_e32 v6, 0x7fffffe, v6
	s_lshl_b32 s0, s17, 4
	v_sub_u32_e32 v5, v5, v6
	s_and_b32 s17, s0, 16
	v_lshl_or_b32 v6, v5, 5, v34
	v_add_u32_e32 v5, s17, v2
	v_and_or_b32 v35, v5, s20, v31
	v_bfe_i32 v7, v35, 0, 22
	v_bfe_u32 v8, v35, 21, 1
	v_add_u32_e32 v8, v7, v8
	v_lshlrev_b32_e32 v9, 3, v8
	v_and_b32_e32 v8, 0x7fffffe, v8
	v_add_u32_e32 v5, 8, v5
	v_sub_u32_e32 v7, v7, v8
	v_and_or_b32 v36, v5, s20, v31
	v_lshl_or_b32 v98, v7, 5, v34
	v_bfe_i32 v5, v36, 0, 22
	v_bfe_u32 v7, v36, 21, 1
	v_add_u32_e32 v7, v5, v7
	v_lshrrev_b32_e32 v33, 6, v32
	v_lshlrev_b32_e32 v8, 3, v7
	v_and_b32_e32 v7, 0x7fffffe, v7
	s_and_b32 s3, s3, 15
	v_and_or_b32 v4, v4, -16, v33
	v_sub_u32_e32 v5, v5, v7
	v_and_or_b32 v14, v9, -16, v33
	v_lshl_or_b32 v100, v5, 5, v34
	v_ashrrev_i32_e32 v5, 31, v4
	s_lshl_b32 s14, s3, 6
	s_lshl_b32 s0, s3, 8
	s_lshl_b32 s2, s3, 7
	v_and_or_b32 v16, v8, -16, v33
	v_lshlrev_b64 v[4:5], 12, v[4:5]
	s_add_u32 s2, s12, s2
	v_ashrrev_i32_e32 v15, 31, v14
	v_lshl_add_u64 v[4:5], s[6:7], 0, v[4:5]
	v_ashrrev_i32_e32 v7, 31, v6
	s_addc_u32 s3, s13, 0
	v_lshlrev_b64 v[102:103], 11, v[14:15]
	v_ashrrev_i32_e32 v99, 31, v98
	v_ashrrev_i32_e32 v17, 31, v16
	v_lshl_add_u64 v[8:9], v[4:5], 0, s[0:1]
	v_lshlrev_b64 v[38:39], 2, v[6:7]
	v_lshl_add_u64 v[14:15], s[2:3], 0, v[102:103]
	v_lshlrev_b64 v[22:23], 1, v[98:99]
	v_lshlrev_b64 v[104:105], 11, v[16:17]
	v_ashrrev_i32_e32 v101, 31, v100
	v_lshl_add_u64 v[18:19], v[8:9], 0, v[38:39]
	v_lshl_add_u64 v[24:25], v[14:15], 0, v[22:23]
	v_lshl_add_u64 v[14:15], s[2:3], 0, v[104:105]
	v_lshlrev_b64 v[26:27], 1, v[100:101]
	global_load_dwordx4 v[6:9], v[18:19], off offset:16
	global_load_dwordx4 v[10:13], v[18:19], off
	v_lshl_add_u64 v[28:29], v[14:15], 0, v[26:27]
	global_load_dwordx4 v[14:17], v[24:25], off
	global_load_dwordx4 v[18:21], v[28:29], off
	v_lshlrev_b32_e32 v24, 10, v30
	v_or_b32_e32 v125, v24, v32
	v_xad_u32 v24, s15, 8, v2
	v_and_or_b32 v24, v24, s20, v31
	v_lshlrev_b32_e32 v25, 10, v24
	v_or_b32_e32 v122, v25, v32
	v_bfe_i32 v25, v24, 0, 22
	v_bfe_u32 v24, v24, 21, 1
	v_add_u32_e32 v28, v25, v24
	v_lshlrev_b32_e32 v24, 3, v28
	v_and_b32_e32 v28, 0x7fffffe, v28
	v_sub_u32_e32 v25, v25, v28
	v_lshl_or_b32 v28, v25, 5, v34
	v_lshlrev_b32_e32 v25, 10, v35
	v_or_b32_e32 v126, v25, v32
	v_lshlrev_b32_e32 v25, 10, v36
	v_or_b32_e32 v127, v25, v32
	v_xad_u32 v25, s17, 16, v2
	v_and_or_b32 v25, v25, s20, v31
	v_lshlrev_b32_e32 v29, 10, v25
	v_or_b32_e32 v123, v29, v32
	v_bfe_i32 v29, v25, 0, 22
	v_bfe_u32 v25, v25, 21, 1
	v_add_u32_e32 v25, v29, v25
	v_and_b32_e32 v121, 3, v2
	v_lshlrev_b32_e32 v30, 3, v25
	v_and_b32_e32 v25, 0x7fffffe, v25
	v_xad_u32 v2, s17, 24, v2
	v_sub_u32_e32 v25, v29, v25
	v_and_or_b32 v2, v2, s20, v31
	v_lshl_or_b32 v106, v25, 5, v34
	v_lshlrev_b32_e32 v25, 10, v2
	v_or_b32_e32 v124, v25, v32
	v_bfe_i32 v25, v2, 0, 22
	v_bfe_u32 v2, v2, 21, 1
	v_add_u32_e32 v2, v25, v2
	v_lshlrev_b32_e32 v29, 3, v2
	v_and_b32_e32 v2, 0x7fffffe, v2
	v_and_b32_e32 v118, 15, v0
	v_sub_u32_e32 v2, v25, v2
	v_lshlrev_b32_e32 v25, 2, v0
	v_ashrrev_i32_e32 v120, 8, v0
	v_and_or_b32 v32, v29, -16, v33
	v_lshl_or_b32 v108, v2, 5, v34
	v_and_b32_e32 v2, 48, v0
	v_and_b32_e32 v25, 32, v25
	v_lshlrev_b32_e32 v29, 6, v118
	v_and_b32_e32 v119, 63, v0
	v_and_or_b32 v24, v24, -16, v33
	v_and_or_b32 v30, v30, -16, v33
	v_lshlrev_b32_e32 v68, 13, v120
	v_bitop3_b32 v2, v29, v25, v2 bitop3:0x36
	v_ashrrev_i32_e32 v25, 31, v24
	v_lshlrev_b64 v[24:25], 12, v[24:25]
	v_lshl_add_u64 v[56:57], s[6:7], 0, v[24:25]
	v_ashrrev_i32_e32 v29, 31, v28
	v_lshl_add_u64 v[24:25], v[56:57], 0, s[0:1]
	v_lshlrev_b64 v[58:59], 2, v[28:29]
	v_ashrrev_i32_e32 v31, 31, v30
	v_lshl_add_u64 v[24:25], v[24:25], 0, v[58:59]
	v_lshlrev_b64 v[110:111], 11, v[30:31]
	v_ashrrev_i32_e32 v107, 31, v106
	v_ashrrev_i32_e32 v33, 31, v32
	global_load_dwordx4 v[40:43], v[24:25], off offset:16
	global_load_dwordx4 v[44:47], v[24:25], off
	v_lshl_add_u64 v[24:25], s[2:3], 0, v[110:111]
	v_lshlrev_b64 v[60:61], 1, v[106:107]
	v_lshlrev_b64 v[112:113], 11, v[32:33]
	v_ashrrev_i32_e32 v109, 31, v108
	v_lshl_add_u64 v[24:25], v[24:25], 0, v[60:61]
	v_lshl_add_u64 v[28:29], s[2:3], 0, v[112:113]
	v_lshlrev_b64 v[62:63], 1, v[108:109]
	v_lshl_add_u64 v[28:29], v[28:29], 0, v[62:63]
	global_load_dwordx4 v[48:51], v[24:25], off
	global_load_dwordx4 v[52:55], v[28:29], off
	s_add_i32 s0, s14, 64
	s_and_b32 s2, s0, 0x3c0
	s_lshl_b32 s0, s2, 2
	s_lshl_b32 s2, s2, 1
	v_lshl_add_u64 v[24:25], v[4:5], 0, s[0:1]
	s_add_u32 s2, s12, s2
	v_lshl_add_u64 v[24:25], v[24:25], 0, v[38:39]
	s_addc_u32 s3, s13, 0
	global_load_dwordx4 v[30:33], v[24:25], off offset:16
	global_load_dwordx4 v[34:37], v[24:25], off
	v_lshl_add_u64 v[24:25], s[2:3], 0, v[102:103]
	v_lshl_add_u64 v[64:65], v[24:25], 0, v[22:23]
	v_lshl_add_u64 v[22:23], s[2:3], 0, v[104:105]
	v_lshl_add_u64 v[66:67], v[22:23], 0, v[26:27]
	global_load_dwordx4 v[26:29], v[64:65], off
	global_load_dwordx4 v[22:25], v[66:67], off
	v_add_u32_e32 v64, 0, v125
	s_waitcnt vmcnt(10)
	v_cvt_pk_bf16_f32 v10, v10, v11
	v_cvt_pk_bf16_f32 v11, v12, v13
	v_cvt_pk_bf16_f32 v12, v6, v7
	v_add_u32_e32 v6, 0, v126
	v_cvt_pk_bf16_f32 v13, v8, v9
	ds_write_b128 v64, v[10:13]
	s_waitcnt vmcnt(9)
	ds_write_b128 v6, v[14:17] offset:32768
	v_add_u32_e32 v6, 0, v127
	s_waitcnt vmcnt(8)
	ds_write_b128 v6, v[18:21] offset:32768
	v_add_u32_e32 v10, 0, v122
	s_waitcnt vmcnt(6)
	v_cvt_pk_bf16_f32 v6, v44, v45
	v_cvt_pk_bf16_f32 v7, v46, v47
	v_cvt_pk_bf16_f32 v8, v40, v41
	v_cvt_pk_bf16_f32 v9, v42, v43
	ds_write_b128 v10, v[6:9]
	v_add_u32_e32 v6, 0, v123
	s_waitcnt vmcnt(5)
	ds_write_b128 v6, v[48:51] offset:32768
	v_add_u32_e32 v6, 0, v124
	s_waitcnt vmcnt(4)
	ds_write_b128 v6, v[52:55] offset:32768
	v_lshl_add_u64 v[6:7], v[56:57], 0, s[0:1]
	v_lshl_add_u64 v[14:15], v[6:7], 0, v[58:59]
	global_load_dwordx4 v[6:9], v[14:15], off offset:16
	global_load_dwordx4 v[10:13], v[14:15], off
	v_lshl_add_u64 v[14:15], s[2:3], 0, v[110:111]
	v_lshl_add_u64 v[40:41], v[14:15], 0, v[60:61]
	v_lshl_add_u64 v[14:15], s[2:3], 0, v[112:113]
	v_lshl_add_u64 v[42:43], v[14:15], 0, v[62:63]
	global_load_dwordx4 v[18:21], v[40:41], off
	global_load_dwordx4 v[14:17], v[42:43], off
	v_lshlrev_b32_e32 v40, 13, v121
	s_cmp_lg_u32 0, -1
	s_waitcnt lgkmcnt(0)
	s_cselect_b32 s0, 0, 0
	v_add3_u32 v128, v68, s0, v2
	s_add_i32 s0, s0, 0x8000
	v_add3_u32 v129, v40, s0, v2
	v_lshl_add_u64 v[114:115], v[4:5], 0, v[38:39]
	v_lshl_add_u64 v[116:117], v[56:57], 0, v[58:59]
	s_add_i32 s2, s14, 0x80
	s_mov_b32 s3, 0
	v_mov_b32_e32 v2, v3
	v_mov_b32_e32 v4, v3
	v_mov_b32_e32 v5, v3
	v_mov_b32_e32 v38, v3
	v_mov_b32_e32 v39, v3
	v_mov_b32_e32 v40, v3
	v_mov_b32_e32 v41, v3
	v_mov_b32_e32 v42, v3
	v_mov_b32_e32 v43, v3
	v_mov_b32_e32 v44, v3
	v_mov_b32_e32 v45, v3
	v_mov_b32_e32 v46, v3
	v_mov_b32_e32 v47, v3
	v_mov_b32_e32 v48, v3
	v_mov_b32_e32 v49, v3
	v_mov_b32_e32 v50, v3
	v_mov_b32_e32 v51, v3
	v_mov_b32_e32 v52, v3
	v_mov_b32_e32 v53, v3
	v_mov_b32_e32 v54, v3
	v_mov_b32_e32 v55, v3
	v_mov_b32_e32 v56, v3
	v_mov_b32_e32 v57, v3
	v_mov_b32_e32 v58, v3
	v_mov_b32_e32 v59, v3
	v_mov_b32_e32 v60, v3
	v_mov_b32_e32 v61, v3
	v_mov_b32_e32 v62, v3
	v_mov_b32_e32 v63, v3
	v_mov_b32_e32 v64, v3
	v_mov_b32_e32 v65, v3
	v_mov_b32_e32 v66, v3
	v_mov_b32_e32 v67, v3
	v_mov_b32_e32 v68, v3
	v_mov_b32_e32 v69, v3
	v_mov_b32_e32 v70, v3
	v_mov_b32_e32 v71, v3
	v_mov_b32_e32 v72, v3
	v_mov_b32_e32 v73, v3
	v_mov_b32_e32 v74, v3
	v_mov_b32_e32 v75, v3
	v_mov_b32_e32 v76, v3
	v_mov_b32_e32 v77, v3
	v_mov_b32_e32 v78, v3
	v_mov_b32_e32 v79, v3
	v_mov_b32_e32 v80, v3
	v_mov_b32_e32 v81, v3
	v_mov_b32_e32 v82, v3
	v_mov_b32_e32 v83, v3
	v_mov_b32_e32 v84, v3
	v_mov_b32_e32 v85, v3
	v_mov_b32_e32 v86, v3
	v_mov_b32_e32 v87, v3
	v_mov_b32_e32 v88, v3
	v_mov_b32_e32 v89, v3
	v_mov_b32_e32 v90, v3
	v_mov_b32_e32 v91, v3
	v_mov_b32_e32 v92, v3
	v_mov_b32_e32 v93, v3
	v_mov_b32_e32 v94, v3
	v_mov_b32_e32 v95, v3
	v_mov_b32_e32 v96, v3
	v_mov_b32_e32 v97, v3
	s_barrier

	.amdhsa_kernel _Z9proj_gemmPKfS0_S0_PK14__hip_bfloat16S0_S0_S0_PS1_
		.amdhsa_group_segment_fixed_size 0
		.amdhsa_private_segment_fixed_size 0
		.amdhsa_kernarg_size 64
		.amdhsa_user_sgpr_count 2
		.amdhsa_user_sgpr_dispatch_ptr 0
		.amdhsa_user_sgpr_queue_ptr 0
		.amdhsa_user_sgpr_kernarg_segment_ptr 1
		.amdhsa_user_sgpr_dispatch_id 0
		.amdhsa_user_sgpr_kernarg_preload_length 0
		.amdhsa_user_sgpr_kernarg_preload_offset 0
		.amdhsa_user_sgpr_private_segment_size 0
		.amdhsa_uses_dynamic_stack 0
		.amdhsa_enable_private_segment 0
		.amdhsa_system_sgpr_workgroup_id_x 1
		.amdhsa_system_sgpr_workgroup_id_y 0
		.amdhsa_system_sgpr_workgroup_id_z 0
		.amdhsa_system_sgpr_workgroup_info 0
		.amdhsa_system_vgpr_workitem_id 0
		.amdhsa_next_free_vgpr 254
		.amdhsa_next_free_sgpr 40
		.amdhsa_accum_offset 256
		.amdhsa_reserve_vcc 0
		.amdhsa_float_round_mode_32 0
		.amdhsa_float_round_mode_16_64 0
		.amdhsa_float_denorm_mode_32 3
		.amdhsa_float_denorm_mode_16_64 3
		.amdhsa_dx10_clamp 1
		.amdhsa_ieee_mode 1
		.amdhsa_fp16_overflow 0
		.amdhsa_tg_split 0
		.amdhsa_exception_fp_ieee_invalid_op 0
		.amdhsa_exception_fp_denorm_src 0
		.amdhsa_exception_fp_ieee_div_zero 0
		.amdhsa_exception_fp_ieee_overflow 0
		.amdhsa_exception_fp_ieee_underflow 0
		.amdhsa_exception_fp_ieee_inexact 0
		.amdhsa_exception_int_div_zero 0
	.end_amdhsa_kernel
